# P7/P8: half-workgroup stagger kept across the unit boundary (no ALIGN idle interval; lagging half defers its last K-loop barrier behind its epilogue and next()), on top of v63
# baseline (speedup 1.0000x reference)
; #define LAS __attribute__((address_space(3)))
; #define PG8_WAIT_V(n) asm volatile("s_waitcnt vmcnt(" #n ")" ::: "memory")
; #define PG8_BAR __builtin_amdgcn_s_barrier()
; template <class Epi, class Sched>
; __device__ __forceinline__ void gemm_phase(LAS unsigned char* lds, const Sched& S, const Epi& E) {
;     ...
;     Unit cur, nxt; int ui = 0;
;     if (!S.next(0, cur)) return;
;     typename Epi::Pre epre;
;     E.prefetch(cur, epre);
;     LAS int* lidx = (LAS int*)(lds + 8 * HTB);
;     if constexpr (Sched::GATHER) {
;         if (tid < 256) { const int v = cur.aidx[tid]; lidx[tid] = (tid < cur.avalid) ? v : 0; }
;         __syncthreads();
;     }
; #pragma unroll
;     for (int h = 0; h < 2; ++h)
; #pragma unroll
;         for (int i = 0; i < 2; ++i) {
;             const int r = h * HALF + sR[i];
;             if constexpr (Sched::GATHER) vA[h][i] = (unsigned)(lidx[r] * RP + sC[i] * 2);
;             else vA[h][i] = (unsigned)(r * RP + sC[i] * 2);
;         }
;     f32x4 acc[2][2][4][2];
; #pragma unroll
;     for (int a = 0; a < 2; ++a)
; #pragma unroll
;         for (int b = 0; b < 2; ++b)
; #pragma unroll
;             for (int m = 0; m < 4; ++m)
; #pragma unroll
;                 for (int n = 0; n < 2; ++n) acc[a][b][m][n] = (f32x4){0.f, 0.f, 0.f, 0.f};
;     i32x8 At[4], B0[2], B1[2];
;     if constexpr (Sched::CRIP & 4) { _Pragma("unroll") for (int m = 0; m < 4; ++m) At[m] = (i32x8){0, 0, 0, 0, 0, 0, 0, 0}; _Pragma("unroll") for (int n = 0; n < 2; ++n) { B0[n] = At[0]; B1[n] = At[0]; } }
;     int f8scale = 0x7f7f7f7f; asm volatile("" : "+v"(f8scale));
;     const char* cA = cur.aBase; const char* cB = cur.bBase;
;     ...
;     int crot = KROT(cur.pm, cur.pn);
;     PG8_STAGE(PG8_SB(0, 0), cB + PG8_KT(crot, 0), voffB); PG8_STAGE(PG8_SB(0, 1), cB + hstep + PG8_KT(crot, 0), voffB); PG8_STAGE(PG8_SA(0, 0), cA + PG8_KT(crot, 0), vA[0]); PG8_STAGE(PG8_SA(0, 1), cA + PG8_KT(crot, 0), vA[1]);
;     if (wr == 1) PG8_BAR;
;     PG8_WAIT_V(2); PG8_BAR;
;     PG8_STAGE(PG8_SB(1, 0), cB + PG8_KT(crot, 1), voffB); PG8_STAGE(PG8_SA(1, 0), cA + PG8_KT(crot, 1), vA[0]); PG8_STAGE(PG8_SB(1, 1), cB + hstep + PG8_KT(crot, 1), voffB);
;     PG8_WAIT_V(6); PG8_BAR;
.LBB0_724:
	s_add_u32 s12, s88, 0x3a800000
	s_addc_u32 s13, s89, 0
	s_lshl_b32 s2, s2, 12
	s_addk_i32 s7, 0x80
	s_lshl_b32 s14, s3, 13
	s_and_b32 s15, s2, 0x3000
	s_and_b32 s7, s7, 0x780
	s_add_u32 s2, s28, s7
	v_mov_b32_e32 v2, v1
	s_waitcnt vmcnt(2)
	s_barrier
	s_addc_u32 s3, s29, 0
	s_add_i32 m0, s39, 0x18000
	v_lshlrev_b32_e32 v3, 6, v0
	global_load_lds_dwordx4 v2, s[2:3]
	v_mov_b32_e32 v2, v190
	s_add_i32 m0, s39, 0x1a000
	v_lshlrev_b32_e32 v5, 2, v0
	global_load_lds_dwordx4 v2, s[2:3]
	s_add_u32 s2, s58, s7
	s_addc_u32 s3, s59, 0
	v_mov_b32_e32 v2, v192
	s_add_i32 s70, s39, 0x8000
	s_mov_b32 m0, s70
	s_add_i32 s71, s39, 0xa000
	global_load_lds_dwordx4 v2, s[2:3]
	v_mov_b32_e32 v2, v194
	s_mov_b32 m0, s71
	v_and_b32_e32 v3, 0x3c0, v3
	global_load_lds_dwordx4 v2, s[2:3]
	s_add_u32 s2, s4, s7
	v_mov_b32_e32 v2, v1
	s_addc_u32 s3, s5, 0
	s_add_i32 m0, s39, 0x1c000
	v_and_b32_e32 v6, 32, v5
	global_load_lds_dwordx4 v2, s[2:3]
	v_mov_b32_e32 v2, v190
	s_add_i32 m0, s39, 0x1e000
	s_cmpk_lt_u32 s6, 0x100
	global_load_lds_dwordx4 v2, s[2:3]
	v_and_b32_e32 v2, 48, v0
	v_or_b32_e32 v4, v3, v2
	v_bitop3_b32 v2, v3, v6, v2 bitop3:0x36
	v_bitop3_b32 v3, s14, v4, v6 bitop3:0xf6
	v_or_b32_e32 v196, s15, v2
	s_cselect_b64 s[14:15], -1, 0
	s_add_i32 s3, 0, 0x27d04
	v_writelane_b32 v255, s3, 55
	s_add_i32 s3, 0, 0x27d4c
	v_writelane_b32 v255, s3, 56
	s_add_i32 s3, 0, 0x27d54
	v_writelane_b32 v255, s3, 57
	s_add_i32 s3, 0, 0x27d5c
	v_writelane_b32 v255, s3, 58
	s_add_i32 s3, 0, 0x27d64
	s_waitcnt vmcnt(0)
	v_writelane_b32 v255, s3, 59
	s_add_i32 s3, 0, 0x27d6c
	s_mov_b32 s4, 0
	s_add_i32 s2, 0, 0x27d80
	v_writelane_b32 v255, s3, 60
	s_add_i32 s3, 0, 0x27d74
	v_mov_b32_e32 v187, 0
	v_add_u32_e32 v197, s60, v5
	s_ashr_i32 s96, s96, 31
	s_add_i32 s9, 0, 0x27d0c
	s_add_i32 s8, 0, 0x27d14
	s_add_i32 s17, 0, 0x27d1c
	s_add_i32 s50, 0, 0x27d24
	s_add_i32 s10, 0, 0x27d2c
	s_add_i32 s11, 0, 0x27d34
	s_add_i32 s56, 0, 0x27d3c
	s_add_i32 s57, 0, 0x27d44
	v_writelane_b32 v255, s3, 61
	s_add_i32 s91, 0, 0x27d7c
	v_lshlrev_b32_e32 v198, 2, v0
	s_add_i32 s92, 0, 0x10000
	s_add_i32 s93, 0, 0x14000
	s_mov_b32 s5, s4
	s_mov_b32 s6, s4
	s_mov_b32 s7, s4
	s_mov_b32 s16, 0xc01d265f
	s_mov_b32 s94, 0xc15083aa
	s_mov_b32 s98, 0xbfd083aa
	v_mov_b32_e32 v199, s2
	v_add_u32_e32 v200, 0, v3
	v_mov_b32_e32 v201, 1
	v_mov_b32_e32 v42, 0xba1d265f
	v_mov_b32_e32 v46, 0xb9d083aa
	v_mov_b32_e32 v202, 0x411c62c0
	v_mov_b32_e32 v188, 0x3fd083aa
	s_mov_b32 s95, s4
	s_mov_b64 s[24:25], s[28:29]
	s_barrier
	v_mov_b32_e32 v4, v0
	s_nop 0
	v_ashrrev_i32_e32 v6, 31, v4
	v_lshrrev_b32_e32 v6, 26, v6
	v_lshlrev_b32_e32 v5, 4, v4
	v_add_u32_e32 v6, v4, v6
	v_bfe_i32 v4, v4, 27, 1
	v_lshrrev_b32_e32 v4, 22, v4
	v_add_u32_e32 v4, v5, v4
	v_and_b32_e32 v4, 0xfffffc00, v4
	v_sub_u32_e32 v4, v5, v4
	v_lshrrev_b32_e32 v7, 4, v4
	v_bitop3_b32 v4, v7, v4, 32 bitop3:0x6c
	v_ashrrev_i32_e32 v7, 31, v4
	v_lshrrev_b32_e32 v7, 26, v7
	v_ashrrev_i32_e32 v6, 6, v6
	v_add_u32_e32 v7, v4, v7
	v_ashrrev_i32_e32 v8, 6, v7
	v_lshlrev_b32_e32 v6, 5, v6
	v_and_b32_e32 v9, 32, v6
	v_and_b32_e32 v10, 0xc0, v7
	v_lshlrev_b32_e32 v7, 2, v8
	v_and_b32_e32 v6, 0xffffffc0, v6
	v_add3_u32 v6, s60, v7, v6
	v_mov_b32_e32 v246, v6
	v_sub_u32_e32 v4, v4, v10
	v_ashrrev_i16_sdwa v4, v201, sext(v4) dst_sel:DWORD dst_unused:UNUSED_PAD src0_sel:DWORD src1_sel:BYTE_0
	v_bfe_i32 v4, v4, 0, 16
	v_add_lshl_u32 v4, v9, v4, 1
	v_mov_b32_e32 v247, v4
	v_add_u32_e32 v4, 0x2000, v5
	v_ashrrev_i32_e32 v5, 31, v4
	v_lshrrev_b32_e32 v5, 22, v5
	v_add_u32_e32 v5, v4, v5
	v_ashrrev_i32_e32 v5, 10, v5
	v_mul_i32_i24_e32 v6, 0x400, v5
	v_sub_u32_e32 v4, v4, v6
	v_lshrrev_b32_e32 v6, 4, v4
	v_bitop3_b32 v4, v6, v4, 32 bitop3:0x6c
	v_ashrrev_i32_e32 v6, 31, v4
	v_lshrrev_b32_e32 v6, 26, v6
	v_add_u32_e32 v6, v4, v6
	v_ashrrev_i32_e32 v7, 6, v6
	v_lshlrev_b32_e32 v5, 5, v5
	v_and_b32_e32 v8, 32, v5
	v_and_b32_e32 v9, 0xc0, v6
	v_lshlrev_b32_e32 v6, 2, v7
	v_and_b32_e32 v5, 0xffffffc0, v5
	v_add3_u32 v5, s60, v6, v5
	v_mov_b32_e32 v248, v5
	v_sub_u32_e32 v4, v4, v9
	v_ashrrev_i16_sdwa v4, v201, sext(v4) dst_sel:DWORD dst_unused:UNUSED_PAD src0_sel:DWORD src1_sel:BYTE_0
	v_bfe_i32 v4, v4, 0, 16
	v_add_lshl_u32 v4, v8, v4, 1
	v_mov_b32_e32 v249, v4
	s_mov_b32 s100, 0
	s_branch .LBB0_727

; #define PG8_STAGE(bufoff, gbase, voff) do { if constexpr (!(Sched::CRIP & 2)) _Pragma("unroll") for (int _i = 0; _i < 2; ++_i) { unsigned _o = (voff)[_i]; asm volatile("" : "+v"(_o)); \
;         __builtin_amdgcn_global_load_lds((const unsigned*)((const char*)(gbase) + _o), (LAS unsigned*)(lds + (bufoff) + ldsw + _i * 8192), 16, 0, 0); } } while (0)
; #define PG8_WAIT_V(n) asm volatile("s_waitcnt vmcnt(" #n ")" ::: "memory")
; #define PG8_WAIT_L(n) asm volatile("s_waitcnt lgkmcnt(" #n ")" ::: "memory")
; template <class Epi, class Sched>
; __device__ __forceinline__ void gemm_phase(LAS unsigned char* lds, const Sched& S, const Epi& E) {
;     ...
;         for (int t = 0; t < nt; t += 2) {
;             const bool last = (t == nt - 2);
;             const char* a1 = cA + PG8_KT(crot, t + 1);
;             const char* a2 = last ? nA + PG8_KT(nrot, 0) : cA + PG8_KT(crot, t + 2); const char* b2 = last ? nB + PG8_KT(nrot, 0) : cB + PG8_KT(crot, t + 2);
;             const char* a3 = last ? nA + PG8_KT(nrot, 1) : cA + PG8_KT(crot, t + 3); const char* b3 = last ? nB + PG8_KT(nrot, 1) : cB + PG8_KT(crot, t + 3);
;             int gi = 0;
;             if constexpr (Sched::GATHER) { if (t == 0 && has_next && tid < 256) gi = nxt.aidx[tid]; }
;             PG8_LDB(B0, 0, 0); PG8_LDB(B1, 0, 1); PG8_SCHED; PG8_LDA(At, 0, 0); PG8_STAGE(PG8_SA(1, 1), a1, vA[1]);
;             PG8_WAIT_V(8); PG8_WAIT_L(0); PG8_BAR; PG8_MMA(0, 0, At, B0); PG8_MMA(0, 1, At, B1); PG8_BAR2; PG8_SCHED;
;             if constexpr (Sched::GATHER) { if (last && has_next) {
;                 int tz = threadIdx.x; asm volatile("" : "+v"(tz));
; #pragma unroll
;                 for (int i = 0; i < 2; ++i) { int R, C; stage_rc(tz * 16 + i * 8192, R, C);
; #pragma unroll
;                     for (int h = 0; h < 2; ++h) vA[h][i] = (unsigned)(lidx[h * HALF + R] * RP + C * 2); } } }
;             PG8_LDA(At, 0, 1); PG8_STAGE(PG8_SB(0, 0), b2, voffB); PG8_STAGE(PG8_SB(0, 1), b2 + hstep, voffB); PG8_STAGE(PG8_SA(0, 0), a2, vA[0]);
;             PG8_WAIT_V(8); PG8_WAIT_L(0); PG8_BAR; PG8_MMA(1, 0, At, B0); PG8_MMA(1, 1, At, B1); PG8_BAR2; PG8_SCHED;
;             PG8_LDB(B0, 1, 0); PG8_LDB(B1, 1, 1); PG8_SCHED; PG8_LDA(At, 1, 0); PG8_STAGE(PG8_SA(0, 1), a2, vA[1]);
;             PG8_WAIT_V(8); PG8_WAIT_L(0); PG8_BAR; PG8_MMA(0, 0, At, B0); PG8_MMA(0, 1, At, B1); PG8_BAR2; PG8_SCHED;
.LBB0_734:
	s_add_i32 s30, s21, 0x80
	s_and_b32 s53, s30, 0x780
	s_and_b64 s[30:31], s[34:35], exec
	s_cselect_b32 s31, s19, s53
	s_cselect_b32 s30, 0, 0
	s_add_u32 s36, s58, s31
	s_addc_u32 s37, s59, s30
	s_add_u32 s53, s28, s53
	s_addc_u32 s54, s29, 0
	s_and_b64 s[30:31], s[34:35], exec
	s_cselect_b32 s55, s46, s54
	s_cselect_b32 s54, s45, s53
	s_addk_i32 s21, 0x100
	s_and_b32 s53, s21, 0x780
	s_and_b64 s[30:31], s[34:35], exec
	s_cselect_b32 s30, s47, s53
	s_cselect_b32 s31, 0, 0
	s_add_u32 s30, s58, s30
	s_addc_u32 s31, s59, s31
	v_mov_b32_e32 v45, v1
	s_mov_b32 m0, s63
	s_add_u32 s53, s28, s53
	ds_read_b128 v[204:207], v200 offset:16384
	ds_read_b128 v[208:211], v200 offset:17408
	ds_read_b128 v[214:217], v200 offset:18432
	ds_read_b128 v[218:221], v200 offset:19456
	ds_read_b128 v[222:225], v200 offset:20480
	ds_read_b128 v[226:229], v200 offset:21504
	ds_read_b128 v[230:233], v200 offset:22528
	ds_read_b128 v[234:237], v200 offset:23552
	s_addc_u32 vcc_lo, s29, 0
	global_load_lds_dwordx4 v45, s[54:55]
	v_mov_b32_e32 v45, v190
	s_and_b64 s[34:35], s[34:35], exec
	s_mov_b32 m0, s64
	s_cselect_b32 s35, s49, vcc_lo
	s_cselect_b32 s34, s48, s53
	global_load_lds_dwordx4 v45, s[54:55]
	s_add_u32 s54, s54, 0x40000
	v_mov_b32_e32 v45, v1
	s_addc_u32 s55, s55, 0
	s_mov_b32 m0, s65
	s_nop 0
	global_load_lds_dwordx4 v45, s[54:55]
	v_mov_b32_e32 v45, v190
	s_mov_b32 m0, s66
	s_nop 0
	global_load_lds_dwordx4 v45, s[54:55]
	v_mov_b32_e32 v45, v192
	s_mov_b32 m0, s39
	s_nop 0
	global_load_lds_dwordx4 v45, s[36:37]
	v_mov_b32_e32 v45, v194
	s_mov_b32 m0, s67
	s_nop 0
	global_load_lds_dwordx4 v45, s[36:37]
	s_waitcnt vmcnt(8)
	s_waitcnt lgkmcnt(0)
	s_barrier
	s_setprio 1
	s_waitcnt lgkmcnt(0)
	s_nop 1
	v_mfma_scale_f32_16x16x128_f8f6f4 v[118:121], v[2:9], v[204:211], v[118:121], v191, v191 op_sel_hi:[0,0,0]
	v_mfma_scale_f32_16x16x128_f8f6f4 v[110:113], v[18:25], v[204:211], v[110:113], v191, v191 op_sel_hi:[0,0,0]
	v_mfma_scale_f32_16x16x128_f8f6f4 v[98:101], v[2:9], v[214:221], v[98:101], v191, v191 op_sel_hi:[0,0,0]
	v_mfma_scale_f32_16x16x128_f8f6f4 v[90:93], v[18:25], v[214:221], v[90:93], v191, v191 op_sel_hi:[0,0,0]
	v_mfma_scale_f32_16x16x128_f8f6f4 v[82:85], v[2:9], v[222:229], v[82:85], v191, v191 op_sel_hi:[0,0,0]
	v_mfma_scale_f32_16x16x128_f8f6f4 v[66:69], v[18:25], v[222:229], v[66:69], v191, v191 op_sel_hi:[0,0,0]
	v_mfma_scale_f32_16x16x128_f8f6f4 v[58:61], v[2:9], v[230:237], v[58:61], v191, v191 op_sel_hi:[0,0,0]
	v_mfma_scale_f32_16x16x128_f8f6f4 v[50:53], v[18:25], v[230:237], v[50:53], v191, v191 op_sel_hi:[0,0,0]
	s_setprio 0
	s_setprio 1
	s_nop 1
	v_mfma_scale_f32_16x16x128_f8f6f4 v[106:109], v[10:17], v[204:211], v[106:109], v191, v191 op_sel_hi:[0,0,0]
	v_mfma_scale_f32_16x16x128_f8f6f4 v[114:117], v[26:33], v[204:211], v[114:117], v191, v191 op_sel_hi:[0,0,0]
	v_mfma_scale_f32_16x16x128_f8f6f4 v[102:105], v[10:17], v[214:221], v[102:105], v191, v191 op_sel_hi:[0,0,0]
	v_mfma_scale_f32_16x16x128_f8f6f4 v[94:97], v[26:33], v[214:221], v[94:97], v191, v191 op_sel_hi:[0,0,0]
	v_mfma_scale_f32_16x16x128_f8f6f4 v[86:89], v[10:17], v[222:229], v[86:89], v191, v191 op_sel_hi:[0,0,0]
	v_mfma_scale_f32_16x16x128_f8f6f4 v[70:73], v[26:33], v[222:229], v[70:73], v191, v191 op_sel_hi:[0,0,0]
	v_mfma_scale_f32_16x16x128_f8f6f4 v[62:65], v[10:17], v[230:237], v[62:65], v191, v191 op_sel_hi:[0,0,0]
	v_mfma_scale_f32_16x16x128_f8f6f4 v[54:57], v[26:33], v[230:237], v[54:57], v191, v191 op_sel_hi:[0,0,0]
	s_setprio 0
	s_barrier
	ds_read_b128 v[2:5], v43
	ds_read_b128 v[6:9], v43 offset:1024
	ds_read_b128 v[10:13], v43 offset:2048
	ds_read_b128 v[14:17], v43 offset:3072
	ds_read_b128 v[18:21], v44
	ds_read_b128 v[22:25], v44 offset:1024
	ds_read_b128 v[26:29], v44 offset:2048
	ds_read_b128 v[30:33], v44 offset:3072
	v_mov_b32_e32 v45, v193
	s_mov_b32 m0, s68
	ds_read_b128 v[204:207], v200 offset:32768
	ds_read_b128 v[208:211], v200 offset:33792
	ds_read_b128 v[214:217], v200 offset:34816
	ds_read_b128 v[218:221], v200 offset:35840
	ds_read_b128 v[222:225], v200 offset:36864
	ds_read_b128 v[226:229], v200 offset:37888
	ds_read_b128 v[230:233], v200 offset:38912
	ds_read_b128 v[234:237], v200 offset:39936
	s_nop 0
	global_load_lds_dwordx4 v45, s[36:37]
	v_mov_b32_e32 v45, v195
	s_mov_b32 m0, s69
	s_nop 0
	global_load_lds_dwordx4 v45, s[36:37]
	s_waitcnt vmcnt(8)
	s_waitcnt lgkmcnt(0)
	s_barrier
; #define PG8_STAGE(bufoff, gbase, voff) do { if constexpr (!(Sched::CRIP & 2)) _Pragma("unroll") for (int _i = 0; _i < 2; ++_i) { unsigned _o = (voff)[_i]; asm volatile("" : "+v"(_o)); \
;         __builtin_amdgcn_global_load_lds((const unsigned*)((const char*)(gbase) + _o), (LAS unsigned*)(lds + (bufoff) + ldsw + _i * 8192), 16, 0, 0); } } while (0)
; #define PG8_LDA(dst, b, h) do { if constexpr (!(Sched::CRIP & 4)) _Pragma("unroll") for (int m = 0; m < 4; ++m) dst[m] = PG8_CAT(*(const LAS i32x4*)(lds + PG8_SA(b, h) + aoff + m * 2048), *(const LAS i32x4*)(lds + PG8_SA(b, h) + aoff + m * 2048 + 1024)); } while (0)
; #define PG8_LDB(dst, b, h) do { if constexpr (!(Sched::CRIP & 4)) _Pragma("unroll") for (int n = 0; n < 2; ++n) dst[n] = PG8_CAT(*(const LAS i32x4*)(lds + PG8_SB(b, h) + boff + n * 2048), *(const LAS i32x4*)(lds + PG8_SB(b, h) + boff + n * 2048 + 1024)); } while (0)
; #define PG8_WAIT_V(n) asm volatile("s_waitcnt vmcnt(" #n ")" ::: "memory")
; #define PG8_WAIT_L(n) asm volatile("s_waitcnt lgkmcnt(" #n ")" ::: "memory")
; #define PG8_BAR __builtin_amdgcn_s_barrier()
; #define PG8_SCHED __builtin_amdgcn_sched_barrier(0)
; template <class Epi, class Sched>
; __device__ __forceinline__ void gemm_phase(LAS unsigned char* lds, const Sched& S, const Epi& E) {
;     ...
;             PG8_WAIT_V(8); PG8_WAIT_L(0); PG8_BAR; PG8_MMA(1, 0, At, B0); PG8_MMA(1, 1, At, B1); PG8_BAR2; PG8_SCHED;
;             PG8_LDB(B0, 1, 0); PG8_LDB(B1, 1, 1); PG8_SCHED; PG8_LDA(At, 1, 0); PG8_STAGE(PG8_SA(0, 1), a2, vA[1]);
;             PG8_WAIT_V(8); PG8_WAIT_L(0); PG8_BAR; PG8_MMA(0, 0, At, B0); PG8_MMA(0, 1, At, B1); PG8_BAR2; PG8_SCHED;
;             PG8_LDA(At, 1, 1); PG8_STAGE(PG8_SB(1, 0), b3, voffB); PG8_STAGE(PG8_SB(1, 1), b3 + hstep, voffB); PG8_STAGE(PG8_SA(1, 0), a3, vA[0]);
;             PG8_WAIT_V(8); PG8_WAIT_L(0); PG8_BAR; PG8_MMA(1, 0, At, B0); PG8_MMA(1, 1, At, B1); PG8_BAR2; PG8_SCHED;
;             if constexpr (Sched::GATHER) { if (t == 0 && has_next && tid < 256) lidx[tid] = (tid < nxt.avalid) ? gi : 0; }
;         }
	s_setprio 1
	s_waitcnt lgkmcnt(0)
	s_nop 1
	v_mfma_scale_f32_16x16x128_f8f6f4 v[178:181], v[2:9], v[204:211], v[178:181], v191, v191 op_sel_hi:[0,0,0]
	v_mfma_scale_f32_16x16x128_f8f6f4 v[170:173], v[10:17], v[204:211], v[170:173], v191, v191 op_sel_hi:[0,0,0]
	v_mfma_scale_f32_16x16x128_f8f6f4 v[162:165], v[2:9], v[214:221], v[162:165], v191, v191 op_sel_hi:[0,0,0]
	v_mfma_scale_f32_16x16x128_f8f6f4 v[154:157], v[10:17], v[214:221], v[154:157], v191, v191 op_sel_hi:[0,0,0]
	v_mfma_scale_f32_16x16x128_f8f6f4 v[146:149], v[2:9], v[222:229], v[146:149], v191, v191 op_sel_hi:[0,0,0]
	v_mfma_scale_f32_16x16x128_f8f6f4 v[138:141], v[10:17], v[222:229], v[138:141], v191, v191 op_sel_hi:[0,0,0]
	v_mfma_scale_f32_16x16x128_f8f6f4 v[130:133], v[2:9], v[230:237], v[130:133], v191, v191 op_sel_hi:[0,0,0]
	v_mfma_scale_f32_16x16x128_f8f6f4 v[122:125], v[10:17], v[230:237], v[122:125], v191, v191 op_sel_hi:[0,0,0]
	s_setprio 0
	s_setprio 1
	s_nop 1
	v_mfma_scale_f32_16x16x128_f8f6f4 v[182:185], v[18:25], v[204:211], v[182:185], v191, v191 op_sel_hi:[0,0,0]
	v_mfma_scale_f32_16x16x128_f8f6f4 v[174:177], v[26:33], v[204:211], v[174:177], v191, v191 op_sel_hi:[0,0,0]
	v_mfma_scale_f32_16x16x128_f8f6f4 v[166:169], v[18:25], v[214:221], v[166:169], v191, v191 op_sel_hi:[0,0,0]
	v_mfma_scale_f32_16x16x128_f8f6f4 v[158:161], v[26:33], v[214:221], v[158:161], v191, v191 op_sel_hi:[0,0,0]
	v_mfma_scale_f32_16x16x128_f8f6f4 v[150:153], v[18:25], v[222:229], v[150:153], v191, v191 op_sel_hi:[0,0,0]
	v_mfma_scale_f32_16x16x128_f8f6f4 v[142:145], v[26:33], v[222:229], v[142:145], v191, v191 op_sel_hi:[0,0,0]
	v_mfma_scale_f32_16x16x128_f8f6f4 v[134:137], v[18:25], v[230:237], v[134:137], v191, v191 op_sel_hi:[0,0,0]
	v_mfma_scale_f32_16x16x128_f8f6f4 v[126:129], v[26:33], v[230:237], v[126:129], v191, v191 op_sel_hi:[0,0,0]
	s_setprio 0
	s_barrier
	v_mov_b32_e32 v45, v1
	s_mov_b32 m0, s40
	ds_read_b128 v[204:207], v200 offset:49152
	ds_read_b128 v[208:211], v200 offset:50176
	ds_read_b128 v[214:217], v200 offset:51200
	ds_read_b128 v[218:221], v200 offset:52224
	ds_read_b128 v[222:225], v200 offset:53248
	ds_read_b128 v[226:229], v200 offset:54272
	ds_read_b128 v[230:233], v200 offset:55296
	ds_read_b128 v[234:237], v200 offset:56320
	s_nop 0
	global_load_lds_dwordx4 v45, s[34:35]
	v_mov_b32_e32 v45, v190
	s_mov_b32 m0, s41
	s_nop 0
	global_load_lds_dwordx4 v45, s[34:35]
	s_add_u32 s34, s34, 0x40000
	v_mov_b32_e32 v45, v1
	s_addc_u32 s35, s35, 0
	s_mov_b32 m0, s42
	s_nop 0
	global_load_lds_dwordx4 v45, s[34:35]
	v_mov_b32_e32 v45, v190
	s_mov_b32 m0, s43
	s_nop 0
	global_load_lds_dwordx4 v45, s[34:35]
	v_mov_b32_e32 v45, v192
	s_mov_b32 m0, s70
	s_nop 0
	global_load_lds_dwordx4 v45, s[30:31]
	v_mov_b32_e32 v45, v194
	s_mov_b32 m0, s71
	s_nop 0
	global_load_lds_dwordx4 v45, s[30:31]
	s_waitcnt vmcnt(8)
	s_waitcnt lgkmcnt(0)
	s_barrier
	s_setprio 1
	s_waitcnt lgkmcnt(0)
	s_nop 1
	v_mfma_scale_f32_16x16x128_f8f6f4 v[118:121], v[2:9], v[204:211], v[118:121], v191, v191 op_sel_hi:[0,0,0]
	v_mfma_scale_f32_16x16x128_f8f6f4 v[110:113], v[10:17], v[204:211], v[110:113], v191, v191 op_sel_hi:[0,0,0]
	v_mfma_scale_f32_16x16x128_f8f6f4 v[98:101], v[2:9], v[214:221], v[98:101], v191, v191 op_sel_hi:[0,0,0]
	v_mfma_scale_f32_16x16x128_f8f6f4 v[90:93], v[10:17], v[214:221], v[90:93], v191, v191 op_sel_hi:[0,0,0]
	v_mfma_scale_f32_16x16x128_f8f6f4 v[82:85], v[2:9], v[222:229], v[82:85], v191, v191 op_sel_hi:[0,0,0]
	v_mfma_scale_f32_16x16x128_f8f6f4 v[66:69], v[10:17], v[222:229], v[66:69], v191, v191 op_sel_hi:[0,0,0]
	v_mfma_scale_f32_16x16x128_f8f6f4 v[58:61], v[2:9], v[230:237], v[58:61], v191, v191 op_sel_hi:[0,0,0]
	v_mfma_scale_f32_16x16x128_f8f6f4 v[50:53], v[10:17], v[230:237], v[50:53], v191, v191 op_sel_hi:[0,0,0]
	s_setprio 0
	s_setprio 1
	s_nop 1
	v_mfma_scale_f32_16x16x128_f8f6f4 v[106:109], v[18:25], v[204:211], v[106:109], v191, v191 op_sel_hi:[0,0,0]
	v_mfma_scale_f32_16x16x128_f8f6f4 v[114:117], v[26:33], v[204:211], v[114:117], v191, v191 op_sel_hi:[0,0,0]
	v_mfma_scale_f32_16x16x128_f8f6f4 v[102:105], v[18:25], v[214:221], v[102:105], v191, v191 op_sel_hi:[0,0,0]
	v_mfma_scale_f32_16x16x128_f8f6f4 v[94:97], v[26:33], v[214:221], v[94:97], v191, v191 op_sel_hi:[0,0,0]
	v_mfma_scale_f32_16x16x128_f8f6f4 v[86:89], v[18:25], v[222:229], v[86:89], v191, v191 op_sel_hi:[0,0,0]
	v_mfma_scale_f32_16x16x128_f8f6f4 v[70:73], v[26:33], v[222:229], v[70:73], v191, v191 op_sel_hi:[0,0,0]
	v_mfma_scale_f32_16x16x128_f8f6f4 v[62:65], v[18:25], v[230:237], v[62:65], v191, v191 op_sel_hi:[0,0,0]
	v_mfma_scale_f32_16x16x128_f8f6f4 v[54:57], v[26:33], v[230:237], v[54:57], v191, v191 op_sel_hi:[0,0,0]
	s_setprio 0
	s_add_i32 s52, s52, 2
	s_cmp_gt_u32 s52, 13
	s_cbranch_scc1 .LBB0_737
	s_barrier

; __device__ __forceinline__ unsigned pk4_fp8(float a, float b, float c, float d) { int v = 0; v = __builtin_amdgcn_cvt_pk_fp8_f32(a, b, v, false); v = __builtin_amdgcn_cvt_pk_fp8_f32(c, d, v, true); return (unsigned)v; }
;     __device__ __forceinline__ void operator()(const f32x4 (&acc)[2][2][4][2], const pg8::Unit& u, const Pre& q, int wr, int wc, int fr, int fq) const {
;         const int row0 = u.pm * 256 + wr * 64 + fr, f0w = u.pn * 128 + wc * 32;
;         constexpr float DS = 1.0f / (FP8_SA * FP8_SW);
;         f32x4 dsk = (f32x4){DS * KP, DS * KP, DS * KP, DS * KP}, dsu = (f32x4){DS, DS, DS, DS}; asm volatile("" : "+v"(dsk), "+v"(dsu));
; #pragma unroll
;         for (int ai = 0; ai < 2; ++ai)
; #pragma unroll
;             for (int mp = 0; mp < 2; ++mp) { unsigned lo[2], hi[2];
; #pragma unroll
;                 for (int mm = 0; mm < 2; ++mm) { const int m = 2 * mp + mm; float h[8];
; #pragma unroll
;                     for (int n = 0; n < 2; ++n) { const f32x4 gk = __builtin_elementwise_fma(acc[ai][0][m][n], dsk, q.bg[n]), up = __builtin_elementwise_fma(acc[ai][1][m][n], dsu, q.bu[n]);
; #pragma unroll
;                         for (int j = 0; j < 4; ++j) { const float gm = __builtin_fmaxf(gk[j], 7.0f * KP), li = __builtin_amdgcn_fmed3f(up[j], -7.0f, 7.0f);
;                             const float sg = __builtin_amdgcn_rcpf(1.0f + __builtin_amdgcn_exp2f(gm));
;                             h[n * 4 + j] = (gm * sg) * (li * (FP8_SH / KP) + (FP8_SH / KP)); } }
;                     lo[mm] = pk4_fp8(h[0], h[1], h[2], h[3]); hi[mm] = pk4_fp8(h[4], h[5], h[6], h[7]); }
;                 const v2u r0 = __builtin_amdgcn_permlane16_swap(lo[0], lo[1], false, false), r1 = __builtin_amdgcn_permlane16_swap(hi[0], hi[1], false, false);
;                 unsigned char* rowp = hb + (size_t)(row0 + ai * 128 + (2 * mp + (fq & 1)) * 16) * FF + f0w + 16 * (fq >> 1);
;                 *(v4u*)rowp = (v4u){r0.x, r1.x, r0.y, r1.y}; }
;     }
.LBB0_739:
	v_mov_b32_e32 v11, v0
	v_mov_b32_e32 v43, v42
	v_readfirstlane_b32 s19, v11
	v_mov_b32_e32 v47, v46
	s_ashr_i32 s27, s19, 2
	v_mov_b32_e32 v44, v42
	v_mov_b32_e32 v45, v42
	v_mov_b32_e32 v48, v46
	v_mov_b32_e32 v49, v46
	v_pk_fma_f32 v[38:39], v[38:39], s[98:99], s[98:99] op_sel_hi:[1,0,0]
	v_pk_fma_f32 v[40:41], v[40:41], s[98:99], s[98:99] op_sel_hi:[1,0,0]
	v_pk_fma_f32 v[34:35], v[34:35], s[98:99], s[98:99] op_sel_hi:[1,0,0]
	v_pk_fma_f32 v[36:37], v[36:37], s[98:99], s[98:99] op_sel_hi:[1,0,0]
	v_mov_b64_e32 v[2:3], v[46:47]
	v_mov_b64_e32 v[6:7], v[42:43]
	v_pk_mul_f32 v[18:19], v[78:79], s[16:17] op_sel_hi:[1,0]
	s_lshl_b32 s21, s38, 8
	s_andn2_b32 s27, s27, 63
	v_mov_b64_e32 v[4:5], v[48:49]
	v_mov_b64_e32 v[8:9], v[44:45]
	s_add_i32 s27, s27, s21
	v_and_or_b32 v10, v11, 31, s27
	v_pk_fma_f32 v[20:21], v[178:179], v[6:7], v[18:19]
	v_lshrrev_b32_e32 v11, 1, v11
	v_max_f32_e32 v23, 0xc1898193, v20
	v_and_b32_e32 v186, 16, v11
	v_exp_f32_e32 v11, v23
	v_max_f32_e32 v21, 0xc1898193, v21
	v_pk_fma_f32 v[28:29], v[182:183], v[2:3], v[38:39]
	v_pk_mul_f32 v[16:17], v[80:81], s[16:17] op_sel_hi:[1,0]
	v_add_f32_e32 v11, 1.0, v11
	v_rcp_f32_e32 v189, v11
	v_exp_f32_e32 v11, v21
	v_med3_f32 v22, v28, s94, v202
	v_pk_fma_f32 v[24:25], v[180:181], v[8:9], v[16:17]
	v_mul_f32_e32 v23, v23, v189
	v_add_f32_e32 v11, 1.0, v11
	v_mul_f32_e32 v30, v22, v23
	v_max_f32_e32 v23, 0xc1898193, v24
	v_rcp_f32_e32 v189, v11
	v_exp_f32_e32 v11, v23
	v_med3_f32 v20, v29, s94, v202
	v_max_f32_e32 v25, 0xc1898193, v25
	v_mul_f32_e32 v21, v21, v189
	v_add_f32_e32 v11, 1.0, v11
	v_rcp_f32_e32 v189, v11
	v_exp_f32_e32 v11, v25
	v_pk_fma_f32 v[26:27], v[184:185], v[4:5], v[40:41]
	v_med3_f32 v22, v26, s94, v202
	v_add_f32_e32 v11, 1.0, v11
	v_mul_f32_e32 v31, v20, v21
	v_mul_f32_e32 v21, v23, v189
	v_rcp_f32_e32 v189, v11
	v_med3_f32 v24, v27, s94, v202
	v_mul_f32_e32 v11, v22, v21
	v_mul_f32_e32 v21, v25, v189
	v_pk_mul_f32 v[14:15], v[74:75], s[16:17] op_sel_hi:[1,0]
	v_mul_f32_e32 v32, v24, v21
	v_pk_fma_f32 v[20:21], v[170:171], v[6:7], v[14:15]
	v_pk_fma_f32 v[28:29], v[174:175], v[2:3], v[34:35]
	v_max_f32_e32 v23, 0xc1898193, v20
	v_exp_f32_e32 v20, v23
	v_max_f32_e32 v21, 0xc1898193, v21
	v_med3_f32 v22, v28, s94, v202
	v_pk_mul_f32 v[12:13], v[76:77], s[16:17] op_sel_hi:[1,0]
	v_add_f32_e32 v20, 1.0, v20
	v_rcp_f32_e32 v189, v20
	v_exp_f32_e32 v20, v21
	v_pk_fma_f32 v[24:25], v[172:173], v[8:9], v[12:13]
	v_pk_fma_f32 v[26:27], v[176:177], v[4:5], v[36:37]
	v_mul_f32_e32 v23, v23, v189
	v_add_f32_e32 v20, 1.0, v20
	v_mul_f32_e32 v28, v22, v23
	v_max_f32_e32 v23, 0xc1898193, v24
	v_exp_f32_e32 v22, v23
	v_rcp_f32_e32 v189, v20
	v_med3_f32 v20, v29, s94, v202
	v_max_f32_e32 v25, 0xc1898193, v25
	v_add_f32_e32 v22, 1.0, v22
	v_mul_f32_e32 v21, v21, v189
	v_rcp_f32_e32 v189, v22
	v_exp_f32_e32 v24, v25
	v_med3_f32 v22, v26, s94, v202
	v_mul_f32_e32 v29, v20, v21
	v_mul_f32_e32 v21, v23, v189
	v_mov_b32_e32 v20, v22
	v_add_f32_e32 v22, 1.0, v24
	v_rcp_f32_e32 v189, v22
	v_mul_f32_e32 v26, v20, v21
	v_med3_f32 v24, v27, s94, v202
	v_cvt_pk_fp8_f32 v21, v28, v29
	v_mul_f32_e32 v23, v25, v189
	v_cvt_pk_fp8_f32 v20, v30, v31
	v_mul_f32_e32 v22, v24, v23
	v_cvt_pk_fp8_f32 v21, v26, v22 op_sel:[0,0,1]
	v_pk_fma_f32 v[22:23], v[162:163], v[6:7], v[18:19]
	v_cvt_pk_fp8_f32 v20, v11, v32 op_sel:[0,0,1]
	v_max_f32_e32 v25, 0xc1898193, v22
	v_exp_f32_e32 v11, v25
	v_max_f32_e32 v23, 0xc1898193, v23
	v_pk_fma_f32 v[30:31], v[166:167], v[2:3], v[38:39]
	v_pk_fma_f32 v[26:27], v[164:165], v[8:9], v[16:17]
	v_add_f32_e32 v11, 1.0, v11
	v_rcp_f32_e32 v189, v11
	v_exp_f32_e32 v11, v23
	v_med3_f32 v24, v30, s94, v202
	v_max_f32_e32 v27, 0xc1898193, v27
	v_mul_f32_e32 v25, v25, v189
	v_add_f32_e32 v11, 1.0, v11
	v_mul_f32_e32 v32, v24, v25
	v_max_f32_e32 v25, 0xc1898193, v26
	v_rcp_f32_e32 v189, v11
	v_exp_f32_e32 v11, v25
	v_med3_f32 v22, v31, s94, v202
	v_pk_fma_f32 v[28:29], v[168:169], v[4:5], v[40:41]
	v_mul_f32_e32 v23, v23, v189
	v_add_f32_e32 v11, 1.0, v11
	v_rcp_f32_e32 v189, v11
	v_exp_f32_e32 v11, v27
	v_med3_f32 v24, v28, s94, v202
	v_mul_f32_e32 v33, v22, v23
	v_add_f32_e32 v11, 1.0, v11
	v_mul_f32_e32 v23, v25, v189
	v_rcp_f32_e32 v189, v11
	v_med3_f32 v26, v29, s94, v202
	v_mul_f32_e32 v11, v24, v23
	v_mul_f32_e32 v23, v27, v189
	v_pk_fma_f32 v[30:31], v[158:159], v[2:3], v[34:35]
	v_mul_f32_e32 v43, v26, v23
	v_pk_fma_f32 v[22:23], v[154:155], v[6:7], v[14:15]
	v_med3_f32 v24, v30, s94, v202
	v_max_f32_e32 v25, 0xc1898193, v22
	v_exp_f32_e32 v22, v25
	v_max_f32_e32 v23, 0xc1898193, v23
	v_pk_fma_f32 v[26:27], v[156:157], v[8:9], v[12:13]
	v_pk_fma_f32 v[28:29], v[160:161], v[4:5], v[36:37]
	v_add_f32_e32 v22, 1.0, v22
	v_rcp_f32_e32 v189, v22
	v_exp_f32_e32 v22, v23
	v_max_f32_e32 v27, 0xc1898193, v27
	s_lshr_b32 s19, s19, 1
	v_mul_f32_e32 v25, v25, v189
	v_add_f32_e32 v22, 1.0, v22
	v_mul_f32_e32 v30, v24, v25
	v_max_f32_e32 v25, 0xc1898193, v26
	v_exp_f32_e32 v24, v25
	v_rcp_f32_e32 v189, v22
	v_med3_f32 v22, v31, s94, v202
	v_exp_f32_e32 v26, v27
	v_add_f32_e32 v24, 1.0, v24
	v_mul_f32_e32 v23, v23, v189
	v_rcp_f32_e32 v189, v24
	v_med3_f32 v24, v28, s94, v202
	v_mul_f32_e32 v31, v22, v23
	v_mul_f32_e32 v23, v25, v189
	v_mov_b32_e32 v22, v24
	v_add_f32_e32 v24, 1.0, v26
	v_rcp_f32_e32 v189, v24
	v_mul_f32_e32 v28, v22, v23
	v_cvt_pk_fp8_f32 v22, v32, v33
	v_med3_f32 v26, v29, s94, v202
	v_cvt_pk_fp8_f32 v23, v30, v31
	v_mul_f32_e32 v25, v27, v189
	v_cvt_pk_fp8_f32 v22, v11, v43 op_sel:[0,0,1]
	v_mul_f32_e32 v11, v26, v25
	s_lshl_b32 s21, s26, 7
	s_and_b32 s19, s19, 0x60
	v_cvt_pk_fp8_f32 v23, v28, v11 op_sel:[0,0,1]
	v_ashrrev_i32_e32 v11, 31, v10
; __device__ __forceinline__ unsigned pk4_fp8(float a, float b, float c, float d) { int v = 0; v = __builtin_amdgcn_cvt_pk_fp8_f32(a, b, v, false); v = __builtin_amdgcn_cvt_pk_fp8_f32(c, d, v, true); return (unsigned)v; }
;     __device__ __forceinline__ void operator()(const f32x4 (&acc)[2][2][4][2], const pg8::Unit& u, const Pre& q, int wr, int wc, int fr, int fq) const {
;         const int row0 = u.pm * 256 + wr * 64 + fr, f0w = u.pn * 128 + wc * 32;
;         constexpr float DS = 1.0f / (FP8_SA * FP8_SW);
;         f32x4 dsk = (f32x4){DS * KP, DS * KP, DS * KP, DS * KP}, dsu = (f32x4){DS, DS, DS, DS}; asm volatile("" : "+v"(dsk), "+v"(dsu));
; #pragma unroll
;         for (int ai = 0; ai < 2; ++ai)
; #pragma unroll
;             for (int mp = 0; mp < 2; ++mp) { unsigned lo[2], hi[2];
; #pragma unroll
;                 for (int mm = 0; mm < 2; ++mm) { const int m = 2 * mp + mm; float h[8];
; #pragma unroll
;                     for (int n = 0; n < 2; ++n) { const f32x4 gk = __builtin_elementwise_fma(acc[ai][0][m][n], dsk, q.bg[n]), up = __builtin_elementwise_fma(acc[ai][1][m][n], dsu, q.bu[n]);
; #pragma unroll
;                         for (int j = 0; j < 4; ++j) { const float gm = __builtin_fmaxf(gk[j], 7.0f * KP), li = __builtin_amdgcn_fmed3f(up[j], -7.0f, 7.0f);
;                             const float sg = __builtin_amdgcn_rcpf(1.0f + __builtin_amdgcn_exp2f(gm));
;                             h[n * 4 + j] = (gm * sg) * (li * (FP8_SH / KP) + (FP8_SH / KP)); } }
;                     lo[mm] = pk4_fp8(h[0], h[1], h[2], h[3]); hi[mm] = pk4_fp8(h[4], h[5], h[6], h[7]); }
;                 const v2u r0 = __builtin_amdgcn_permlane16_swap(lo[0], lo[1], false, false), r1 = __builtin_amdgcn_permlane16_swap(hi[0], hi[1], false, false);
;                 unsigned char* rowp = hb + (size_t)(row0 + ai * 128 + (2 * mp + (fq & 1)) * 16) * FF + f0w + 16 * (fq >> 1);
;                 *(v4u*)rowp = (v4u){r0.x, r1.x, r0.y, r1.y}; }
;     }
	s_or_b32 s26, s19, s21
	v_lshlrev_b64 v[24:25], 11, v[10:11]
	s_ashr_i32 s27, s26, 31
	v_lshl_add_u64 v[24:25], s[12:13], 0, v[24:25]
	v_lshl_add_u64 v[24:25], v[24:25], 0, s[26:27]
	v_permlane16_swap_b32_e32 v20, v22
	v_permlane16_swap_b32_e32 v21, v23
	v_lshl_add_u64 v[24:25], v[24:25], 0, v[186:187]
	global_store_dwordx4 v[24:25], v[20:23], off
	v_pk_fma_f32 v[28:29], v[150:151], v[2:3], v[38:39]
	v_pk_fma_f32 v[24:25], v[148:149], v[8:9], v[16:17]
	v_pk_fma_f32 v[20:21], v[146:147], v[6:7], v[18:19]
	v_med3_f32 v22, v28, s94, v202
	v_max_f32_e32 v23, 0xc1898193, v20
	v_exp_f32_e32 v11, v23
	v_max_f32_e32 v21, 0xc1898193, v21
	v_max_f32_e32 v25, 0xc1898193, v25
	v_pk_fma_f32 v[26:27], v[152:153], v[4:5], v[40:41]
	v_add_f32_e32 v11, 1.0, v11
	v_rcp_f32_e32 v189, v11
	v_exp_f32_e32 v11, v21
	s_andn2_b64 vcc, exec, s[2:3]
	s_mov_b64 s[2:3], -1
	v_mul_f32_e32 v23, v23, v189
	v_add_f32_e32 v11, 1.0, v11
	v_mul_f32_e32 v30, v22, v23
	v_max_f32_e32 v23, 0xc1898193, v24
	v_rcp_f32_e32 v189, v11
	v_exp_f32_e32 v11, v23
	v_med3_f32 v20, v29, s94, v202
	v_med3_f32 v22, v26, s94, v202
	v_mul_f32_e32 v21, v21, v189
	v_add_f32_e32 v11, 1.0, v11
	v_rcp_f32_e32 v189, v11
	v_exp_f32_e32 v11, v25
	v_mul_f32_e32 v31, v20, v21
	v_mul_f32_e32 v21, v23, v189
	v_add_f32_e32 v11, 1.0, v11
	v_rcp_f32_e32 v189, v11
	v_med3_f32 v24, v27, s94, v202
	v_mul_f32_e32 v11, v22, v21
	v_mul_f32_e32 v21, v25, v189
	v_pk_fma_f32 v[28:29], v[142:143], v[2:3], v[34:35]
	v_mul_f32_e32 v32, v24, v21
	v_pk_fma_f32 v[20:21], v[138:139], v[6:7], v[14:15]
	v_med3_f32 v22, v28, s94, v202
	v_max_f32_e32 v23, 0xc1898193, v20
	v_exp_f32_e32 v20, v23
	v_max_f32_e32 v21, 0xc1898193, v21
	v_pk_fma_f32 v[24:25], v[140:141], v[8:9], v[12:13]
	v_pk_fma_f32 v[26:27], v[144:145], v[4:5], v[36:37]
	v_add_f32_e32 v20, 1.0, v20
	v_rcp_f32_e32 v189, v20
	v_exp_f32_e32 v20, v21
	v_max_f32_e32 v25, 0xc1898193, v25
	v_mul_f32_e32 v23, v23, v189
	s_nop 0
	v_mul_f32_e32 v28, v22, v23
	v_max_f32_e32 v23, 0xc1898193, v24
	v_add_f32_e32 v20, 1.0, v20
	v_exp_f32_e32 v22, v23
	v_rcp_f32_e32 v189, v20
	v_med3_f32 v20, v29, s94, v202
	v_exp_f32_e32 v24, v25
	v_add_f32_e32 v22, 1.0, v22
	v_mul_f32_e32 v21, v21, v189
	v_rcp_f32_e32 v189, v22
	v_med3_f32 v22, v26, s94, v202
	v_mul_f32_e32 v29, v20, v21
	v_mul_f32_e32 v21, v23, v189
	v_mov_b32_e32 v20, v22
	v_add_f32_e32 v22, 1.0, v24
	v_rcp_f32_e32 v189, v22
	v_mul_f32_e32 v26, v20, v21
	v_med3_f32 v24, v27, s94, v202
	v_cvt_pk_fp8_f32 v21, v28, v29
	v_mul_f32_e32 v23, v25, v189
	v_cvt_pk_fp8_f32 v20, v30, v31
	v_mul_f32_e32 v22, v24, v23
	v_cvt_pk_fp8_f32 v21, v26, v22 op_sel:[0,0,1]
	v_pk_fma_f32 v[22:23], v[130:131], v[6:7], v[18:19]
	v_cvt_pk_fp8_f32 v20, v11, v32 op_sel:[0,0,1]
	v_max_f32_e32 v25, 0xc1898193, v22
	v_exp_f32_e32 v11, v25
	v_max_f32_e32 v23, 0xc1898193, v23
	v_pk_fma_f32 v[30:31], v[134:135], v[2:3], v[38:39]
	v_pk_fma_f32 v[26:27], v[132:133], v[8:9], v[16:17]
	v_add_f32_e32 v11, 1.0, v11
	v_rcp_f32_e32 v189, v11
	v_exp_f32_e32 v11, v23
	v_med3_f32 v24, v30, s94, v202
	v_max_f32_e32 v27, 0xc1898193, v27
	v_mul_f32_e32 v25, v25, v189
	v_add_f32_e32 v11, 1.0, v11
	v_mul_f32_e32 v32, v24, v25
	v_max_f32_e32 v25, 0xc1898193, v26
	v_rcp_f32_e32 v189, v11
	v_exp_f32_e32 v11, v25
	v_med3_f32 v22, v31, s94, v202
	v_pk_fma_f32 v[28:29], v[136:137], v[4:5], v[40:41]
	v_mul_f32_e32 v23, v23, v189
	v_add_f32_e32 v11, 1.0, v11
	v_rcp_f32_e32 v189, v11
	v_exp_f32_e32 v11, v27
	v_med3_f32 v24, v28, s94, v202
	v_mul_f32_e32 v33, v22, v23
	v_add_f32_e32 v11, 1.0, v11
	v_mul_f32_e32 v23, v25, v189
	v_rcp_f32_e32 v189, v11
	v_med3_f32 v26, v29, s94, v202
	v_mul_f32_e32 v11, v24, v23
	v_mul_f32_e32 v23, v27, v189
	v_pk_fma_f32 v[30:31], v[126:127], v[2:3], v[34:35]
	v_mul_f32_e32 v43, v26, v23
	v_pk_fma_f32 v[22:23], v[122:123], v[6:7], v[14:15]
	v_med3_f32 v24, v30, s94, v202
	v_max_f32_e32 v25, 0xc1898193, v22
	v_exp_f32_e32 v22, v25
	v_max_f32_e32 v23, 0xc1898193, v23
	v_pk_fma_f32 v[26:27], v[124:125], v[8:9], v[12:13]
	v_pk_fma_f32 v[28:29], v[128:129], v[4:5], v[36:37]
	v_add_f32_e32 v22, 1.0, v22
	v_rcp_f32_e32 v189, v22
	v_exp_f32_e32 v22, v23
	v_max_f32_e32 v27, 0xc1898193, v27
	v_mul_f32_e32 v25, v25, v189
	s_nop 0
	v_mul_f32_e32 v30, v24, v25
	v_max_f32_e32 v25, 0xc1898193, v26
	v_add_f32_e32 v22, 1.0, v22
	v_exp_f32_e32 v24, v25
	v_rcp_f32_e32 v189, v22
	v_med3_f32 v22, v31, s94, v202
	v_exp_f32_e32 v26, v27
	v_add_f32_e32 v24, 1.0, v24
	v_mul_f32_e32 v23, v23, v189
	v_rcp_f32_e32 v189, v24
	v_med3_f32 v24, v28, s94, v202
	v_mul_f32_e32 v31, v22, v23
	v_mul_f32_e32 v23, v25, v189
	v_mov_b32_e32 v22, v24
	v_add_f32_e32 v24, 1.0, v26
	v_rcp_f32_e32 v189, v24
	v_mul_f32_e32 v28, v22, v23
	v_cvt_pk_fp8_f32 v22, v32, v33
	v_med3_f32 v26, v29, s94, v202
	v_cvt_pk_fp8_f32 v23, v30, v31
	v_mul_f32_e32 v25, v27, v189
	v_cvt_pk_fp8_f32 v22, v11, v43 op_sel:[0,0,1]
	v_mul_f32_e32 v11, v26, v25
	v_or_b32_e32 v24, 32, v10
	v_cvt_pk_fp8_f32 v23, v28, v11 op_sel:[0,0,1]
	v_ashrrev_i32_e32 v25, 31, v24
	v_lshlrev_b64 v[24:25], 11, v[24:25]
	v_lshl_add_u64 v[24:25], s[12:13], 0, v[24:25]
	v_lshl_add_u64 v[24:25], v[24:25], 0, s[26:27]
	v_permlane16_swap_b32_e32 v20, v22
	v_permlane16_swap_b32_e32 v21, v23
	v_lshl_add_u64 v[24:25], v[24:25], 0, v[186:187]
	global_store_dwordx4 v[24:25], v[20:23], off
	v_pk_fma_f32 v[30:31], v[106:107], v[2:3], v[38:39]
	v_pk_fma_f32 v[26:27], v[120:121], v[8:9], v[16:17]
	v_pk_fma_f32 v[22:23], v[118:119], v[6:7], v[18:19]
	v_med3_f32 v24, v30, s94, v202
	v_max_f32_e32 v25, 0xc1898193, v22
	v_exp_f32_e32 v11, v25
	v_max_f32_e32 v23, 0xc1898193, v23
	v_med3_f32 v22, v31, s94, v202
	v_max_f32_e32 v27, 0xc1898193, v27
; __device__ __forceinline__ unsigned pk4_fp8(float a, float b, float c, float d) { int v = 0; v = __builtin_amdgcn_cvt_pk_fp8_f32(a, b, v, false); v = __builtin_amdgcn_cvt_pk_fp8_f32(c, d, v, true); return (unsigned)v; }
;     __device__ __forceinline__ void operator()(const f32x4 (&acc)[2][2][4][2], const pg8::Unit& u, const Pre& q, int wr, int wc, int fr, int fq) const {
;         const int row0 = u.pm * 256 + wr * 64 + fr, f0w = u.pn * 128 + wc * 32;
;         constexpr float DS = 1.0f / (FP8_SA * FP8_SW);
;         f32x4 dsk = (f32x4){DS * KP, DS * KP, DS * KP, DS * KP}, dsu = (f32x4){DS, DS, DS, DS}; asm volatile("" : "+v"(dsk), "+v"(dsu));
; #pragma unroll
;         for (int ai = 0; ai < 2; ++ai)
; #pragma unroll
;             for (int mp = 0; mp < 2; ++mp) { unsigned lo[2], hi[2];
; #pragma unroll
;                 for (int mm = 0; mm < 2; ++mm) { const int m = 2 * mp + mm; float h[8];
; #pragma unroll
;                     for (int n = 0; n < 2; ++n) { const f32x4 gk = __builtin_elementwise_fma(acc[ai][0][m][n], dsk, q.bg[n]), up = __builtin_elementwise_fma(acc[ai][1][m][n], dsu, q.bu[n]);
; #pragma unroll
;                         for (int j = 0; j < 4; ++j) { const float gm = __builtin_fmaxf(gk[j], 7.0f * KP), li = __builtin_amdgcn_fmed3f(up[j], -7.0f, 7.0f);
;                             const float sg = __builtin_amdgcn_rcpf(1.0f + __builtin_amdgcn_exp2f(gm));
;                             h[n * 4 + j] = (gm * sg) * (li * (FP8_SH / KP) + (FP8_SH / KP)); } }
;                     lo[mm] = pk4_fp8(h[0], h[1], h[2], h[3]); hi[mm] = pk4_fp8(h[4], h[5], h[6], h[7]); }
;                 const v2u r0 = __builtin_amdgcn_permlane16_swap(lo[0], lo[1], false, false), r1 = __builtin_amdgcn_permlane16_swap(hi[0], hi[1], false, false);
;                 unsigned char* rowp = hb + (size_t)(row0 + ai * 128 + (2 * mp + (fq & 1)) * 16) * FF + f0w + 16 * (fq >> 1);
;                 *(v4u*)rowp = (v4u){r0.x, r1.x, r0.y, r1.y}; }
;     }
	v_add_f32_e32 v11, 1.0, v11
	v_rcp_f32_e32 v189, v11
	v_exp_f32_e32 v11, v23
	v_pk_fma_f32 v[28:29], v[108:109], v[4:5], v[40:41]
	v_pk_fma_f32 v[30:31], v[114:115], v[2:3], v[34:35]
	v_mul_f32_e32 v25, v25, v189
	v_add_f32_e32 v11, 1.0, v11
	v_mul_f32_e32 v21, v24, v25
	v_max_f32_e32 v25, 0xc1898193, v26
	v_rcp_f32_e32 v189, v11
	v_exp_f32_e32 v11, v25
	v_med3_f32 v24, v28, s94, v202
	v_med3_f32 v26, v29, s94, v202
	v_mul_f32_e32 v23, v23, v189
	v_add_f32_e32 v11, 1.0, v11
	v_rcp_f32_e32 v189, v11
	v_exp_f32_e32 v11, v27
	v_mul_f32_e32 v32, v22, v23
	v_mul_f32_e32 v23, v25, v189
	v_add_f32_e32 v11, 1.0, v11
	v_rcp_f32_e32 v189, v11
	v_mul_f32_e32 v11, v24, v23
	v_med3_f32 v24, v30, s94, v202
	v_mul_f32_e32 v23, v27, v189
	v_mov_b32_e32 v22, v26
	v_pk_fma_f32 v[26:27], v[112:113], v[8:9], v[12:13]
	v_mul_f32_e32 v33, v22, v23
	v_pk_fma_f32 v[22:23], v[110:111], v[6:7], v[14:15]
	v_max_f32_e32 v27, 0xc1898193, v27
	v_max_f32_e32 v25, 0xc1898193, v22
	v_exp_f32_e32 v22, v25
	v_max_f32_e32 v23, 0xc1898193, v23
	v_pk_fma_f32 v[28:29], v[116:117], v[4:5], v[36:37]
	v_add_u32_e32 v20, 0x80, v10
	v_add_f32_e32 v22, 1.0, v22
	v_rcp_f32_e32 v189, v22
	v_exp_f32_e32 v22, v23
	v_mul_f32_e32 v25, v25, v189
	s_nop 0
	v_mul_f32_e32 v30, v24, v25
	v_max_f32_e32 v25, 0xc1898193, v26
	v_add_f32_e32 v22, 1.0, v22
	v_exp_f32_e32 v24, v25
	v_rcp_f32_e32 v189, v22
	v_med3_f32 v22, v31, s94, v202
	v_exp_f32_e32 v26, v27
	v_add_f32_e32 v24, 1.0, v24
	v_mul_f32_e32 v23, v23, v189
	v_rcp_f32_e32 v189, v24
	v_med3_f32 v24, v28, s94, v202
	v_mul_f32_e32 v31, v22, v23
	v_mul_f32_e32 v23, v25, v189
	v_mov_b32_e32 v22, v24
	v_add_f32_e32 v24, 1.0, v26
	v_rcp_f32_e32 v189, v24
	v_mul_f32_e32 v28, v22, v23
	v_med3_f32 v26, v29, s94, v202
	v_mul_f32_e32 v25, v27, v189
	v_cvt_pk_fp8_f32 v22, v21, v32
	v_mul_f32_e32 v21, v26, v25
	v_pk_fma_f32 v[24:25], v[98:99], v[6:7], v[18:19]
	v_cvt_pk_fp8_f32 v22, v11, v33 op_sel:[0,0,1]
	v_max_f32_e32 v27, 0xc1898193, v24
	v_exp_f32_e32 v11, v27
	v_cvt_pk_fp8_f32 v23, v30, v31
	v_max_f32_e32 v25, 0xc1898193, v25
	v_add_f32_e32 v11, 1.0, v11
	v_rcp_f32_e32 v189, v11
	v_pk_fma_f32 v[32:33], v[102:103], v[2:3], v[38:39]
	v_exp_f32_e32 v11, v25
	v_med3_f32 v26, v32, s94, v202
	v_mul_f32_e32 v27, v27, v189
	v_cvt_pk_fp8_f32 v23, v28, v21 op_sel:[0,0,1]
	v_pk_fma_f32 v[28:29], v[100:101], v[8:9], v[16:17]
	v_mul_f32_e32 v21, v26, v27
	v_add_f32_e32 v11, 1.0, v11
	v_max_f32_e32 v27, 0xc1898193, v28
	v_rcp_f32_e32 v189, v11
	v_exp_f32_e32 v11, v27
	v_med3_f32 v24, v33, s94, v202
	v_max_f32_e32 v29, 0xc1898193, v29
	v_mul_f32_e32 v25, v25, v189
	v_add_f32_e32 v11, 1.0, v11
	v_rcp_f32_e32 v189, v11
	v_exp_f32_e32 v11, v29
	v_pk_fma_f32 v[30:31], v[104:105], v[4:5], v[40:41]
	v_med3_f32 v26, v30, s94, v202
	v_add_f32_e32 v11, 1.0, v11
	v_mul_f32_e32 v43, v24, v25
	v_mul_f32_e32 v25, v27, v189
	v_rcp_f32_e32 v189, v11
	v_med3_f32 v28, v31, s94, v202
	v_mul_f32_e32 v11, v26, v25
	v_mul_f32_e32 v25, v29, v189
	v_pk_fma_f32 v[32:33], v[94:95], v[2:3], v[34:35]
	v_mul_f32_e32 v44, v28, v25
	v_pk_fma_f32 v[24:25], v[90:91], v[6:7], v[14:15]
	v_med3_f32 v26, v32, s94, v202
	v_max_f32_e32 v27, 0xc1898193, v24
	v_exp_f32_e32 v24, v27
	v_max_f32_e32 v25, 0xc1898193, v25
	v_pk_fma_f32 v[28:29], v[92:93], v[8:9], v[12:13]
	v_pk_fma_f32 v[30:31], v[96:97], v[4:5], v[36:37]
	v_add_f32_e32 v24, 1.0, v24
	v_rcp_f32_e32 v189, v24
	v_exp_f32_e32 v24, v25
	v_max_f32_e32 v29, 0xc1898193, v29
	v_mul_f32_e32 v27, v27, v189
	s_nop 0
	v_mul_f32_e32 v32, v26, v27
	v_max_f32_e32 v27, 0xc1898193, v28
	v_add_f32_e32 v24, 1.0, v24
	v_exp_f32_e32 v26, v27
	v_rcp_f32_e32 v189, v24
	v_med3_f32 v24, v33, s94, v202
	v_exp_f32_e32 v28, v29
	v_add_f32_e32 v26, 1.0, v26
	v_mul_f32_e32 v25, v25, v189
	v_rcp_f32_e32 v189, v26
	v_med3_f32 v26, v30, s94, v202
	v_mul_f32_e32 v33, v24, v25
	v_mul_f32_e32 v25, v27, v189
	v_mov_b32_e32 v24, v26
	v_add_f32_e32 v26, 1.0, v28
	v_rcp_f32_e32 v189, v26
	v_mul_f32_e32 v30, v24, v25
	v_cvt_pk_fp8_f32 v24, v21, v43
	v_med3_f32 v28, v31, s94, v202
	v_cvt_pk_fp8_f32 v25, v32, v33
	v_mul_f32_e32 v27, v29, v189
	v_cvt_pk_fp8_f32 v24, v11, v44 op_sel:[0,0,1]
	v_mul_f32_e32 v11, v28, v27
	v_cvt_pk_fp8_f32 v25, v30, v11 op_sel:[0,0,1]
	v_ashrrev_i32_e32 v21, 31, v20
	v_lshlrev_b64 v[20:21], 11, v[20:21]
	v_lshl_add_u64 v[20:21], s[12:13], 0, v[20:21]
	v_lshl_add_u64 v[20:21], v[20:21], 0, s[26:27]
	v_permlane16_swap_b32_e32 v22, v24
	v_permlane16_swap_b32_e32 v23, v25
	v_lshl_add_u64 v[20:21], v[20:21], 0, v[186:187]
	global_store_dwordx4 v[20:21], v[22:25], off
	v_pk_fma_f32 v[20:21], v[82:83], v[6:7], v[18:19]
	v_pk_fma_f32 v[28:29], v[86:87], v[2:3], v[38:39]
	v_max_f32_e32 v23, 0xc1898193, v20
	v_exp_f32_e32 v11, v23
	v_max_f32_e32 v21, 0xc1898193, v21
	v_med3_f32 v22, v28, s94, v202
	v_pk_fma_f32 v[24:25], v[84:85], v[8:9], v[16:17]
	v_add_f32_e32 v11, 1.0, v11
	v_rcp_f32_e32 v189, v11
	v_exp_f32_e32 v11, v21
	v_max_f32_e32 v25, 0xc1898193, v25
	v_pk_fma_f32 v[26:27], v[88:89], v[4:5], v[40:41]
	v_mul_f32_e32 v23, v23, v189
	v_add_f32_e32 v11, 1.0, v11
	v_mul_f32_e32 v30, v22, v23
	v_max_f32_e32 v23, 0xc1898193, v24
	v_rcp_f32_e32 v189, v11
	v_exp_f32_e32 v11, v23
	v_med3_f32 v20, v29, s94, v202
	v_med3_f32 v22, v26, s94, v202
	v_mul_f32_e32 v21, v21, v189
	v_add_f32_e32 v11, 1.0, v11
	v_rcp_f32_e32 v189, v11
; template <class Epi, class Sched>
; __device__ __forceinline__ void gemm_phase(LAS unsigned char* lds, const Sched& S, const Epi& E) {
;     ...
;         cur = nxt; cA = nA; cB = nB; crot = nrot; ++ui;
;     __device__ __forceinline__ void prefetch(const pg8::Unit& u, Pre& q) const {
;         int tz = threadIdx.x; asm volatile("" : "+v"(tz)); const int wc = (tz >> 6) & 3, fq = (tz >> 4) & 3;
;         const int f0 = u.pn * 128 + wc * 32 + 8 * fq;
; #pragma unroll
;         for (int n = 0; n < 2; ++n) { q.bg[n] = *(const f32x4*)(b_gate + (size_t)u.e * FF + f0 + 4 * n) * KP; q.bu[n] = *(const f32x4*)(b_up + (size_t)u.e * FF + f0 + 4 * n); }
;     }
;     __device__ __forceinline__ void operator()(const f32x4 (&acc)[2][2][4][2], const pg8::Unit& u, const Pre& q, int wr, int wc, int fr, int fq) const {
;         const int row0 = u.pm * 256 + wr * 64 + fr, f0w = u.pn * 128 + wc * 32;
;         constexpr float DS = 1.0f / (FP8_SA * FP8_SW);
;         f32x4 dsk = (f32x4){DS * KP, DS * KP, DS * KP, DS * KP}, dsu = (f32x4){DS, DS, DS, DS}; asm volatile("" : "+v"(dsk), "+v"(dsu));
; #pragma unroll
;         for (int ai = 0; ai < 2; ++ai)
; #pragma unroll
;             for (int mp = 0; mp < 2; ++mp) { unsigned lo[2], hi[2];
; #pragma unroll
;                 for (int mm = 0; mm < 2; ++mm) { const int m = 2 * mp + mm; float h[8];
; #pragma unroll
;                     for (int n = 0; n < 2; ++n) { const f32x4 gk = __builtin_elementwise_fma(acc[ai][0][m][n], dsk, q.bg[n]), up = __builtin_elementwise_fma(acc[ai][1][m][n], dsu, q.bu[n]);
; #pragma unroll
;                         for (int j = 0; j < 4; ++j) { const float gm = __builtin_fmaxf(gk[j], 7.0f * KP), li = __builtin_amdgcn_fmed3f(up[j], -7.0f, 7.0f);
;                             const float sg = __builtin_amdgcn_rcpf(1.0f + __builtin_amdgcn_exp2f(gm));
;                             h[n * 4 + j] = (gm * sg) * (li * (FP8_SH / KP) + (FP8_SH / KP)); } }
;                     lo[mm] = pk4_fp8(h[0], h[1], h[2], h[3]); hi[mm] = pk4_fp8(h[4], h[5], h[6], h[7]); }
;                 const v2u r0 = __builtin_amdgcn_permlane16_swap(lo[0], lo[1], false, false), r1 = __builtin_amdgcn_permlane16_swap(hi[0], hi[1], false, false);
;                 unsigned char* rowp = hb + (size_t)(row0 + ai * 128 + (2 * mp + (fq & 1)) * 16) * FF + f0w + 16 * (fq >> 1);
;                 *(v4u*)rowp = (v4u){r0.x, r1.x, r0.y, r1.y}; }
;     }
	v_exp_f32_e32 v11, v25
	v_mul_f32_e32 v31, v20, v21
	v_mul_f32_e32 v21, v23, v189
	v_add_f32_e32 v11, 1.0, v11
	v_rcp_f32_e32 v189, v11
	v_med3_f32 v24, v27, s94, v202
	v_mul_f32_e32 v11, v22, v21
	v_mul_f32_e32 v21, v25, v189
	v_pk_fma_f32 v[28:29], v[70:71], v[2:3], v[34:35]
	v_mul_f32_e32 v32, v24, v21
	v_pk_fma_f32 v[20:21], v[66:67], v[6:7], v[14:15]
	v_med3_f32 v22, v28, s94, v202
	v_max_f32_e32 v23, 0xc1898193, v20
	v_exp_f32_e32 v20, v23
	v_max_f32_e32 v21, 0xc1898193, v21
	v_pk_fma_f32 v[24:25], v[68:69], v[8:9], v[12:13]
	v_pk_fma_f32 v[26:27], v[72:73], v[4:5], v[36:37]
	v_add_f32_e32 v20, 1.0, v20
	v_rcp_f32_e32 v189, v20
	v_exp_f32_e32 v20, v21
	v_max_f32_e32 v25, 0xc1898193, v25
	v_pk_fma_f32 v[18:19], v[58:59], v[6:7], v[18:19]
	v_mul_f32_e32 v23, v23, v189
	v_add_f32_e32 v20, 1.0, v20
	v_mul_f32_e32 v28, v22, v23
	v_max_f32_e32 v23, 0xc1898193, v24
	v_exp_f32_e32 v22, v23
	v_rcp_f32_e32 v189, v20
	v_med3_f32 v20, v29, s94, v202
	v_exp_f32_e32 v24, v25
	v_add_f32_e32 v22, 1.0, v22
	v_mul_f32_e32 v21, v21, v189
	v_rcp_f32_e32 v189, v22
	v_med3_f32 v22, v26, s94, v202
	v_mul_f32_e32 v29, v20, v21
	v_mul_f32_e32 v21, v23, v189
	v_mov_b32_e32 v20, v22
	v_add_f32_e32 v22, 1.0, v24
	v_rcp_f32_e32 v189, v22
	v_mul_f32_e32 v26, v20, v21
	v_med3_f32 v24, v27, s94, v202
	v_cvt_pk_fp8_f32 v20, v30, v31
	v_mul_f32_e32 v23, v25, v189
	v_mul_f32_e32 v22, v24, v23
	v_max_f32_e32 v23, 0xc1898193, v18
	v_cvt_pk_fp8_f32 v20, v11, v32 op_sel:[0,0,1]
	v_exp_f32_e32 v11, v23
	v_cvt_pk_fp8_f32 v21, v28, v29
	v_max_f32_e32 v19, 0xc1898193, v19
	v_pk_fma_f32 v[16:17], v[60:61], v[8:9], v[16:17]
	v_add_f32_e32 v11, 1.0, v11
	v_rcp_f32_e32 v189, v11
	v_cvt_pk_fp8_f32 v21, v26, v22 op_sel:[0,0,1]
	v_pk_fma_f32 v[26:27], v[62:63], v[2:3], v[38:39]
	v_exp_f32_e32 v11, v19
	v_med3_f32 v22, v26, s94, v202
	v_mul_f32_e32 v23, v23, v189
	v_max_f32_e32 v17, 0xc1898193, v17
	v_mul_f32_e32 v26, v22, v23
	v_add_f32_e32 v11, 1.0, v11
	v_max_f32_e32 v23, 0xc1898193, v16
	v_rcp_f32_e32 v189, v11
	v_exp_f32_e32 v11, v23
	v_med3_f32 v18, v27, s94, v202
	v_pk_fma_f32 v[6:7], v[50:51], v[6:7], v[14:15]
	v_mul_f32_e32 v19, v19, v189
	v_add_f32_e32 v11, 1.0, v11
	v_rcp_f32_e32 v189, v11
	v_exp_f32_e32 v11, v17
	v_pk_fma_f32 v[24:25], v[64:65], v[4:5], v[40:41]
	v_max_f32_e32 v15, 0xc1898193, v6
	v_med3_f32 v22, v24, s94, v202
	v_add_f32_e32 v11, 1.0, v11
	v_exp_f32_e32 v6, v15
	v_mul_f32_e32 v27, v18, v19
	v_mul_f32_e32 v19, v23, v189
	v_mov_b32_e32 v18, v22
	v_rcp_f32_e32 v189, v11
	v_med3_f32 v16, v25, s94, v202
	v_add_f32_e32 v6, 1.0, v6
	v_pk_fma_f32 v[2:3], v[54:55], v[2:3], v[34:35]
	v_mul_f32_e32 v17, v17, v189
	v_rcp_f32_e32 v189, v6
	v_max_f32_e32 v7, 0xc1898193, v7
	v_med3_f32 v14, v2, s94, v202
	v_exp_f32_e32 v2, v7
	v_pk_fma_f32 v[8:9], v[52:53], v[8:9], v[12:13]
	v_mul_f32_e32 v13, v15, v189
	v_pk_fma_f32 v[4:5], v[56:57], v[4:5], v[36:37]
	v_mul_f32_e32 v14, v14, v13
	v_add_f32_e32 v2, 1.0, v2
	v_max_f32_e32 v13, 0xc1898193, v8
	v_rcp_f32_e32 v189, v2
	v_exp_f32_e32 v8, v13
	v_med3_f32 v6, v3, s94, v202
	v_med3_f32 v12, v4, s94, v202
	v_mul_f32_e32 v3, v7, v189
	v_mov_b32_e32 v2, v6
	v_add_f32_e32 v6, 1.0, v8
	v_max_f32_e32 v7, 0xc1898193, v9
	v_rcp_f32_e32 v189, v6
	v_exp_f32_e32 v6, v7
	v_mul_f32_e32 v8, v2, v3
	v_mul_f32_e32 v3, v13, v189
	v_add_f32_e32 v4, 1.0, v6
	v_rcp_f32_e32 v189, v4
	v_med3_f32 v6, v5, s94, v202
	v_cvt_pk_fp8_f32 v23, v14, v8
	v_mul_f32_e32 v4, v12, v3
	v_mul_f32_e32 v3, v7, v189
	v_cvt_pk_fp8_f32 v22, v26, v27
	v_mul_f32_e32 v2, v6, v3
	v_mul_f32_e32 v11, v18, v19
	v_mul_f32_e32 v16, v16, v17
	v_cvt_pk_fp8_f32 v23, v4, v2 op_sel:[0,0,1]
	v_add_u32_e32 v2, 0xa0, v10
	v_cvt_pk_fp8_f32 v22, v11, v16 op_sel:[0,0,1]
	v_ashrrev_i32_e32 v3, 31, v2
	v_lshlrev_b64 v[2:3], 11, v[2:3]
	v_lshl_add_u64 v[2:3], s[12:13], 0, v[2:3]
	v_lshl_add_u64 v[2:3], v[2:3], 0, s[26:27]
	v_permlane16_swap_b32_e32 v20, v22
	v_permlane16_swap_b32_e32 v21, v23
	v_lshl_add_u64 v[2:3], v[2:3], 0, v[186:187]
	global_store_dwordx4 v[2:3], v[20:23], off
	s_cbranch_vccnz .LBB0_726
	v_mov_b32_e32 v2, v0
	s_ashr_i32 s21, s20, 31
	v_readlane_b32 s72, v255, 29
	v_lshrrev_b32_e32 v2, 1, v2
	s_lshl_b64 s[2:3], s[20:21], 13
	v_readlane_b32 s76, v255, 33
	v_and_b32_e32 v2, 0x78, v2
	v_readlane_b32 s77, v255, 34
	s_add_u32 s26, s76, s2
	v_lshl_or_b32 v2, s44, 7, v2
	v_readlane_b32 s80, v255, 37
	s_addc_u32 s27, s77, s3
	v_ashrrev_i32_e32 v3, 31, v2
	v_readlane_b32 s81, v255, 38
	s_add_u32 s2, s80, s2
	v_lshlrev_b64 v[2:3], 2, v[2:3]
	s_addc_u32 s3, s81, s3
	v_lshl_add_u64 v[4:5], s[26:27], 0, v[2:3]
	v_lshl_add_u64 v[2:3], s[2:3], 0, v[2:3]
	global_load_dwordx4 v[74:77], v[4:5], off offset:16
	global_load_dwordx4 v[78:81], v[4:5], off
	global_load_dwordx4 v[34:37], v[2:3], off offset:16
	global_load_dwordx4 v[38:41], v[2:3], off
	v_readlane_b32 s2, v255, 53
	v_readlane_b32 s3, v255, 54
	s_andn2_b64 vcc, exec, s[2:3]
	v_readlane_b32 s73, v255, 30
	v_readlane_b32 s74, v255, 31
	v_readlane_b32 s75, v255, 32
	v_readlane_b32 s78, v255, 35
	v_readlane_b32 s79, v255, 36
	v_readlane_b32 s82, v255, 39
	v_readlane_b32 s83, v255, 40
	v_readlane_b32 s84, v255, 41
	v_readlane_b32 s85, v255, 42
	v_readlane_b32 s86, v255, 43
	v_readlane_b32 s87, v255, 44
	s_mov_b32 s100, 0
	s_cbranch_vccnz .LBB0_725
	s_mov_b32 s100, 1
	s_branch .LBB0_725

; #define PG8_STAGE(bufoff, gbase, voff) do { if constexpr (!(Sched::CRIP & 2)) _Pragma("unroll") for (int _i = 0; _i < 2; ++_i) { unsigned _o = (voff)[_i]; asm volatile("" : "+v"(_o)); \
;         __builtin_amdgcn_global_load_lds((const unsigned*)((const char*)(gbase) + _o), (LAS unsigned*)(lds + (bufoff) + ldsw + _i * 8192), 16, 0, 0); } } while (0)
; #define PG8_LDA(dst, b, h) do { if constexpr (!(Sched::CRIP & 4)) _Pragma("unroll") for (int m = 0; m < 4; ++m) dst[m] = PG8_CAT(*(const LAS i32x4*)(lds + PG8_SA(b, h) + aoff + m * 2048), *(const LAS i32x4*)(lds + PG8_SA(b, h) + aoff + m * 2048 + 1024)); } while (0)
; #define PG8_LDB(dst, b, h) do { if constexpr (!(Sched::CRIP & 4)) _Pragma("unroll") for (int n = 0; n < 2; ++n) dst[n] = PG8_CAT(*(const LAS i32x4*)(lds + PG8_SB(b, h) + boff + n * 2048), *(const LAS i32x4*)(lds + PG8_SB(b, h) + boff + n * 2048 + 1024)); } while (0)
; #define PG8_WAIT_V(n) asm volatile("s_waitcnt vmcnt(" #n ")" ::: "memory")
; #define PG8_WAIT_L(n) asm volatile("s_waitcnt lgkmcnt(" #n ")" ::: "memory")
; #define PG8_BAR __builtin_amdgcn_s_barrier()
; template <class Epi, class Sched>
; __device__ __forceinline__ void gemm_phase(LAS unsigned char* lds, const Sched& S, const Epi& E) {
;     ...
;             PG8_LDB(B0, 0, 0); PG8_LDB(B1, 0, 1); PG8_SCHED; PG8_LDA(At, 0, 0); PG8_STAGE(PG8_SA(1, 1), a1, vA[1]);
;             PG8_WAIT_V(8); PG8_WAIT_L(0); PG8_BAR; PG8_MMA(0, 0, At, B0); PG8_MMA(0, 1, At, B1); PG8_BAR2; PG8_SCHED;
;             if constexpr (Sched::GATHER) { if (last && has_next) {
;                 int tz = threadIdx.x; asm volatile("" : "+v"(tz));
; #pragma unroll
;                 for (int i = 0; i < 2; ++i) { int R, C; stage_rc(tz * 16 + i * 8192, R, C);
; #pragma unroll
;                     for (int h = 0; h < 2; ++h) vA[h][i] = (unsigned)(lidx[h * HALF + R] * RP + C * 2); } } }
;             PG8_LDA(At, 0, 1); PG8_STAGE(PG8_SB(0, 0), b2, voffB); PG8_STAGE(PG8_SB(0, 1), b2 + hstep, voffB); PG8_STAGE(PG8_SA(0, 0), a2, vA[0]);
;             PG8_WAIT_V(8); PG8_WAIT_L(0); PG8_BAR; PG8_MMA(1, 0, At, B0); PG8_MMA(1, 1, At, B1); PG8_BAR2; PG8_SCHED;
;             PG8_LDB(B0, 1, 0); PG8_LDB(B1, 1, 1); PG8_SCHED; PG8_LDA(At, 1, 0); PG8_STAGE(PG8_SA(0, 1), a2, vA[1]);
;             PG8_WAIT_V(8); PG8_WAIT_L(0); PG8_BAR; PG8_MMA(0, 0, At, B0); PG8_MMA(0, 1, At, B1); PG8_BAR2; PG8_SCHED;
.Lstag8:
	s_and_b32 s13, s12, 15
	s_and_b64 s[30:31], s[0:1], exec
	s_cselect_b32 s15, s13, s34
	s_lshl_b32 s30, s15, 7
	s_add_u32 s15, s92, s30
	s_addc_u32 s17, s93, 0
	s_add_u32 s25, s94, s30
	s_addc_u32 s38, s95, 0
	s_addk_i32 s30, 0x80
	s_and_b32 s30, s30, 0x780
	s_add_u32 s39, s92, s30
	s_addc_u32 s80, s93, 0
	s_add_u32 s81, s94, s30
	s_addc_u32 s82, s95, 0
	s_lshl_b32 s30, s34, 7
	s_add_i32 s83, s30, 0x180
	s_mov_b32 s84, -2
	s_add_i32 s30, s83, 0xffffff00
	s_add_i32 s31, s83, 0xffffff80
	s_and_b32 s30, s30, 0x780
	s_and_b32 s31, s31, 0x780
	s_add_u32 s34, s26, s31
	s_addc_u32 s35, s27, 0
	s_add_u32 s40, s28, s31
	s_addc_u32 s41, s29, 0
	s_and_b32 s31, s83, 0x780
	s_add_u32 s53, s26, s31
	v_add_u32_e32 v2, s77, v186
	v_add_u32_e32 v22, s78, v186
	s_addc_u32 s85, s27, 0
	ds_read_b128 v[10:13], v2
	ds_read_b128 v[14:17], v2 offset:1024
	ds_read_b128 v[26:29], v2 offset:2048
	ds_read_b128 v[30:33], v2 offset:3072
	ds_read_b128 v[2:5], v22
	ds_read_b128 v[6:9], v22 offset:1024
	ds_read_b128 v[18:21], v22 offset:2048
	ds_read_b128 v[22:25], v22 offset:3072
	s_add_u32 s36, s28, s31
	s_addc_u32 s37, s29, 0
	s_add_u32 s54, s26, s30
	s_addc_u32 s55, s27, 0
	s_add_i32 s87, s77, s47
	s_add_i32 m0, s69, 0xc000
	s_add_i32 s86, s69, 0xe000
	s_add_i32 s52, s87, 0x2000
	s_cmp_eq_u32 s84, 12
	s_cselect_b32 s35, s17, s35
	s_cselect_b32 s34, s15, s34
	s_cselect_b32 s31, s80, s85
	s_cselect_b32 s30, s39, s53
	s_cselect_b32 s41, s38, s41
	s_cselect_b32 s40, s25, s40
	v_mov_b32_e32 v178, v183
	ds_read_b128 v[198:201], v188
	ds_read_b128 v[202:205], v188 offset:1024
	ds_read_b128 v[214:217], v188 offset:2048
	ds_read_b128 v[218:221], v188 offset:3072
	ds_read_b128 v[222:225], v188 offset:4096
	ds_read_b128 v[226:229], v188 offset:5120
	ds_read_b128 v[230:233], v188 offset:6144
	ds_read_b128 v[234:237], v188 offset:7168
	s_nop 0
	global_load_lds_dwordx4 v178, s[54:55]
	v_mov_b32_e32 v178, v184
	s_mov_b32 m0, s86
	s_nop 0
	global_load_lds_dwordx4 v178, s[54:55]
	s_waitcnt vmcnt(28)
	s_waitcnt lgkmcnt(0)
	s_barrier
	s_setprio 1
	s_waitcnt lgkmcnt(0)
	s_nop 1
	v_mfma_scale_f32_16x16x128_f8f6f4 v[174:177], v[10:17], v[198:205], 0, v185, v185 op_sel_hi:[0,0,0]
	v_mfma_scale_f32_16x16x128_f8f6f4 v[170:173], v[26:33], v[198:205], 0, v185, v185 op_sel_hi:[0,0,0]
	v_mfma_scale_f32_16x16x128_f8f6f4 v[166:169], v[10:17], v[214:221], 0, v185, v185 op_sel_hi:[0,0,0]
	v_mfma_scale_f32_16x16x128_f8f6f4 v[162:165], v[26:33], v[214:221], 0, v185, v185 op_sel_hi:[0,0,0]
	v_mfma_scale_f32_16x16x128_f8f6f4 v[142:145], v[10:17], v[222:229], 0, v185, v185 op_sel_hi:[0,0,0]
	v_mfma_scale_f32_16x16x128_f8f6f4 v[138:141], v[26:33], v[222:229], 0, v185, v185 op_sel_hi:[0,0,0]
	v_mfma_scale_f32_16x16x128_f8f6f4 v[134:137], v[10:17], v[230:237], 0, v185, v185 op_sel_hi:[0,0,0]
	v_mfma_scale_f32_16x16x128_f8f6f4 v[130:133], v[26:33], v[230:237], 0, v185, v185 op_sel_hi:[0,0,0]
	s_setprio 0
	s_setprio 1
	s_nop 1
	v_mfma_scale_f32_16x16x128_f8f6f4 v[158:161], v[2:9], v[198:205], 0, v185, v185 op_sel_hi:[0,0,0]
	v_mfma_scale_f32_16x16x128_f8f6f4 v[154:157], v[18:25], v[198:205], 0, v185, v185 op_sel_hi:[0,0,0]
	v_mfma_scale_f32_16x16x128_f8f6f4 v[150:153], v[2:9], v[214:221], 0, v185, v185 op_sel_hi:[0,0,0]
	v_mfma_scale_f32_16x16x128_f8f6f4 v[146:149], v[18:25], v[214:221], 0, v185, v185 op_sel_hi:[0,0,0]
	v_mfma_scale_f32_16x16x128_f8f6f4 v[126:129], v[2:9], v[222:229], 0, v185, v185 op_sel_hi:[0,0,0]
	v_mfma_scale_f32_16x16x128_f8f6f4 v[122:125], v[18:25], v[222:229], 0, v185, v185 op_sel_hi:[0,0,0]
	v_mfma_scale_f32_16x16x128_f8f6f4 v[118:121], v[2:9], v[230:237], 0, v185, v185 op_sel_hi:[0,0,0]
	v_mfma_scale_f32_16x16x128_f8f6f4 v[114:117], v[18:25], v[230:237], 0, v185, v185 op_sel_hi:[0,0,0]
	s_setprio 0
	s_barrier
	v_mov_b32_e32 v178, v1
	s_mov_b32 m0, s87
	ds_read_b128 v[198:201], v188 offset:16384
	ds_read_b128 v[202:205], v188 offset:17408
	ds_read_b128 v[214:217], v188 offset:18432
	ds_read_b128 v[218:221], v188 offset:19456
	ds_read_b128 v[222:225], v188 offset:20480
	ds_read_b128 v[226:229], v188 offset:21504
	ds_read_b128 v[230:233], v188 offset:22528
	ds_read_b128 v[234:237], v188 offset:23552
	s_cselect_b32 s36, s81, s36
	global_load_lds_dwordx4 v178, s[40:41]
	v_mov_b32_e32 v178, v180
	s_mov_b32 m0, s52
	s_cselect_b32 s37, s82, s37
	global_load_lds_dwordx4 v178, s[40:41]
	s_add_u32 s40, s40, 0x40000
	v_mov_b32_e32 v178, v1
	s_addc_u32 s41, s41, 0
	s_add_i32 s52, s78, s47
	s_mov_b32 m0, s52
	s_nop 0
	global_load_lds_dwordx4 v178, s[40:41]
	v_mov_b32_e32 v178, v180
	s_add_i32 m0, s52, 0x2000
	s_nop 0
	global_load_lds_dwordx4 v178, s[40:41]
	v_mov_b32_e32 v178, v181
	s_mov_b32 m0, s69
	s_nop 0
	global_load_lds_dwordx4 v178, s[34:35]
	v_mov_b32_e32 v178, v182
	s_mov_b32 m0, s70
	s_nop 0
	global_load_lds_dwordx4 v178, s[34:35]
	s_waitcnt vmcnt(28)
	s_waitcnt lgkmcnt(0)
	s_barrier
; #define PG8_STAGE(bufoff, gbase, voff) do { if constexpr (!(Sched::CRIP & 2)) _Pragma("unroll") for (int _i = 0; _i < 2; ++_i) { unsigned _o = (voff)[_i]; asm volatile("" : "+v"(_o)); \
;         __builtin_amdgcn_global_load_lds((const unsigned*)((const char*)(gbase) + _o), (LAS unsigned*)(lds + (bufoff) + ldsw + _i * 8192), 16, 0, 0); } } while (0)
; #define PG8_LDA(dst, b, h) do { if constexpr (!(Sched::CRIP & 4)) _Pragma("unroll") for (int m = 0; m < 4; ++m) dst[m] = PG8_CAT(*(const LAS i32x4*)(lds + PG8_SA(b, h) + aoff + m * 2048), *(const LAS i32x4*)(lds + PG8_SA(b, h) + aoff + m * 2048 + 1024)); } while (0)
; #define PG8_LDB(dst, b, h) do { if constexpr (!(Sched::CRIP & 4)) _Pragma("unroll") for (int n = 0; n < 2; ++n) dst[n] = PG8_CAT(*(const LAS i32x4*)(lds + PG8_SB(b, h) + boff + n * 2048), *(const LAS i32x4*)(lds + PG8_SB(b, h) + boff + n * 2048 + 1024)); } while (0)
; #define PG8_WAIT_V(n) asm volatile("s_waitcnt vmcnt(" #n ")" ::: "memory")
; #define PG8_WAIT_L(n) asm volatile("s_waitcnt lgkmcnt(" #n ")" ::: "memory")
; #define PG8_BAR __builtin_amdgcn_s_barrier()
; #define PG8_SCHED __builtin_amdgcn_sched_barrier(0)
; template <class Epi, class Sched>
; __device__ __forceinline__ void gemm_phase(LAS unsigned char* lds, const Sched& S, const Epi& E) {
;     ...
;             PG8_WAIT_V(8); PG8_WAIT_L(0); PG8_BAR; PG8_MMA(1, 0, At, B0); PG8_MMA(1, 1, At, B1); PG8_BAR2; PG8_SCHED;
;             PG8_LDB(B0, 1, 0); PG8_LDB(B1, 1, 1); PG8_SCHED; PG8_LDA(At, 1, 0); PG8_STAGE(PG8_SA(0, 1), a2, vA[1]);
;             PG8_WAIT_V(8); PG8_WAIT_L(0); PG8_BAR; PG8_MMA(0, 0, At, B0); PG8_MMA(0, 1, At, B1); PG8_BAR2; PG8_SCHED;
;             PG8_LDA(At, 1, 1); PG8_STAGE(PG8_SB(1, 0), b3, voffB); PG8_STAGE(PG8_SB(1, 1), b3 + hstep, voffB); PG8_STAGE(PG8_SA(1, 0), a3, vA[0]);
;             PG8_WAIT_V(8); PG8_WAIT_L(0); PG8_BAR; PG8_MMA(1, 0, At, B0); PG8_MMA(1, 1, At, B1); PG8_BAR2; PG8_SCHED;
	s_setprio 1
	s_waitcnt lgkmcnt(0)
	s_nop 1
	v_mfma_scale_f32_16x16x128_f8f6f4 v[110:113], v[10:17], v[198:205], 0, v185, v185 op_sel_hi:[0,0,0]
	v_mfma_scale_f32_16x16x128_f8f6f4 v[106:109], v[26:33], v[198:205], 0, v185, v185 op_sel_hi:[0,0,0]
	v_mfma_scale_f32_16x16x128_f8f6f4 v[102:105], v[10:17], v[214:221], 0, v185, v185 op_sel_hi:[0,0,0]
	v_mfma_scale_f32_16x16x128_f8f6f4 v[98:101], v[26:33], v[214:221], 0, v185, v185 op_sel_hi:[0,0,0]
	v_mfma_scale_f32_16x16x128_f8f6f4 v[78:81], v[10:17], v[222:229], 0, v185, v185 op_sel_hi:[0,0,0]
	v_mfma_scale_f32_16x16x128_f8f6f4 v[74:77], v[26:33], v[222:229], 0, v185, v185 op_sel_hi:[0,0,0]
	v_mfma_scale_f32_16x16x128_f8f6f4 v[70:73], v[10:17], v[230:237], 0, v185, v185 op_sel_hi:[0,0,0]
	v_mfma_scale_f32_16x16x128_f8f6f4 v[66:69], v[26:33], v[230:237], 0, v185, v185 op_sel_hi:[0,0,0]
	s_setprio 0
	s_setprio 1
	s_nop 1
	v_mfma_scale_f32_16x16x128_f8f6f4 v[94:97], v[2:9], v[198:205], 0, v185, v185 op_sel_hi:[0,0,0]
	v_mfma_scale_f32_16x16x128_f8f6f4 v[90:93], v[18:25], v[198:205], 0, v185, v185 op_sel_hi:[0,0,0]
	v_mfma_scale_f32_16x16x128_f8f6f4 v[86:89], v[2:9], v[214:221], 0, v185, v185 op_sel_hi:[0,0,0]
	v_mfma_scale_f32_16x16x128_f8f6f4 v[82:85], v[18:25], v[214:221], 0, v185, v185 op_sel_hi:[0,0,0]
	v_mfma_scale_f32_16x16x128_f8f6f4 v[62:65], v[2:9], v[222:229], 0, v185, v185 op_sel_hi:[0,0,0]
	v_mfma_scale_f32_16x16x128_f8f6f4 v[58:61], v[18:25], v[222:229], 0, v185, v185 op_sel_hi:[0,0,0]
	v_mfma_scale_f32_16x16x128_f8f6f4 v[54:57], v[2:9], v[230:237], 0, v185, v185 op_sel_hi:[0,0,0]
	v_mfma_scale_f32_16x16x128_f8f6f4 v[50:53], v[18:25], v[230:237], 0, v185, v185 op_sel_hi:[0,0,0]
	s_setprio 0
	s_barrier
	s_add_i32 s40, 0, 0x18000
	s_add_i32 s41, 0, 0x1c000
	v_add_u32_e32 v14, s40, v186
	v_add_u32_e32 v30, s41, v186
	ds_read_b128 v[2:5], v14
	ds_read_b128 v[6:9], v14 offset:1024
	ds_read_b128 v[10:13], v14 offset:2048
	ds_read_b128 v[14:17], v14 offset:3072
	ds_read_b128 v[18:21], v30
	ds_read_b128 v[22:25], v30 offset:1024
	ds_read_b128 v[26:29], v30 offset:2048
	ds_read_b128 v[30:33], v30 offset:3072
	v_mov_b32_e32 v178, v183
	s_mov_b32 m0, s71
	ds_read_b128 v[198:201], v188 offset:32768
	ds_read_b128 v[202:205], v188 offset:33792
	ds_read_b128 v[214:217], v188 offset:34816
	ds_read_b128 v[218:221], v188 offset:35840
	ds_read_b128 v[222:225], v188 offset:36864
	ds_read_b128 v[226:229], v188 offset:37888
	ds_read_b128 v[230:233], v188 offset:38912
	ds_read_b128 v[234:237], v188 offset:39936
	s_nop 0
	global_load_lds_dwordx4 v178, s[34:35]
	v_mov_b32_e32 v178, v184
	s_mov_b32 m0, s72
	s_nop 0
	global_load_lds_dwordx4 v178, s[34:35]
	s_waitcnt vmcnt(8)
	s_waitcnt lgkmcnt(0)
	s_barrier
	s_setprio 1
	s_waitcnt lgkmcnt(0)
	s_nop 1
	v_mfma_scale_f32_16x16x128_f8f6f4 v[174:177], v[2:9], v[198:205], v[174:177], v185, v185 op_sel_hi:[0,0,0]
	v_mfma_scale_f32_16x16x128_f8f6f4 v[170:173], v[10:17], v[198:205], v[170:173], v185, v185 op_sel_hi:[0,0,0]
	v_mfma_scale_f32_16x16x128_f8f6f4 v[166:169], v[2:9], v[214:221], v[166:169], v185, v185 op_sel_hi:[0,0,0]
	v_mfma_scale_f32_16x16x128_f8f6f4 v[162:165], v[10:17], v[214:221], v[162:165], v185, v185 op_sel_hi:[0,0,0]
	v_mfma_scale_f32_16x16x128_f8f6f4 v[142:145], v[2:9], v[222:229], v[142:145], v185, v185 op_sel_hi:[0,0,0]
	v_mfma_scale_f32_16x16x128_f8f6f4 v[138:141], v[10:17], v[222:229], v[138:141], v185, v185 op_sel_hi:[0,0,0]
	v_mfma_scale_f32_16x16x128_f8f6f4 v[134:137], v[2:9], v[230:237], v[134:137], v185, v185 op_sel_hi:[0,0,0]
	v_mfma_scale_f32_16x16x128_f8f6f4 v[130:133], v[10:17], v[230:237], v[130:133], v185, v185 op_sel_hi:[0,0,0]
	s_setprio 0
	s_setprio 1
	s_nop 1
	v_mfma_scale_f32_16x16x128_f8f6f4 v[158:161], v[18:25], v[198:205], v[158:161], v185, v185 op_sel_hi:[0,0,0]
	v_mfma_scale_f32_16x16x128_f8f6f4 v[154:157], v[26:33], v[198:205], v[154:157], v185, v185 op_sel_hi:[0,0,0]
	v_mfma_scale_f32_16x16x128_f8f6f4 v[150:153], v[18:25], v[214:221], v[150:153], v185, v185 op_sel_hi:[0,0,0]
	v_mfma_scale_f32_16x16x128_f8f6f4 v[146:149], v[26:33], v[214:221], v[146:149], v185, v185 op_sel_hi:[0,0,0]
	v_mfma_scale_f32_16x16x128_f8f6f4 v[126:129], v[18:25], v[222:229], v[126:129], v185, v185 op_sel_hi:[0,0,0]
	v_mfma_scale_f32_16x16x128_f8f6f4 v[122:125], v[26:33], v[222:229], v[122:125], v185, v185 op_sel_hi:[0,0,0]
	v_mfma_scale_f32_16x16x128_f8f6f4 v[118:121], v[18:25], v[230:237], v[118:121], v185, v185 op_sel_hi:[0,0,0]
	v_mfma_scale_f32_16x16x128_f8f6f4 v[114:117], v[26:33], v[230:237], v[114:117], v185, v185 op_sel_hi:[0,0,0]
	s_setprio 0
	s_barrier
	v_mov_b32_e32 v178, v1
	s_add_i32 s34, s40, s47
	ds_read_b128 v[198:201], v188 offset:49152
	ds_read_b128 v[202:205], v188 offset:50176
	ds_read_b128 v[214:217], v188 offset:51200
	ds_read_b128 v[218:221], v188 offset:52224
	ds_read_b128 v[222:225], v188 offset:53248
	ds_read_b128 v[226:229], v188 offset:54272
	ds_read_b128 v[230:233], v188 offset:55296
	ds_read_b128 v[234:237], v188 offset:56320
	s_mov_b32 m0, s34
	s_nop 0
	global_load_lds_dwordx4 v178, s[36:37]
	v_mov_b32_e32 v178, v180
	s_add_i32 m0, s34, 0x2000
	s_add_u32 s34, s36, 0x40000
	global_load_lds_dwordx4 v178, s[36:37]
	s_addc_u32 s35, s37, 0
	v_mov_b32_e32 v178, v1
	s_add_i32 s36, s41, s47
	s_mov_b32 m0, s36
	s_nop 0
	global_load_lds_dwordx4 v178, s[34:35]
	v_mov_b32_e32 v178, v180
	s_add_i32 m0, s36, 0x2000
	s_nop 0
	global_load_lds_dwordx4 v178, s[34:35]
	v_mov_b32_e32 v178, v181
	s_mov_b32 m0, s74
	s_nop 0
	global_load_lds_dwordx4 v178, s[30:31]
	v_mov_b32_e32 v178, v182
	s_mov_b32 m0, s75
	s_nop 0
	global_load_lds_dwordx4 v178, s[30:31]
	s_waitcnt vmcnt(8)
	s_waitcnt lgkmcnt(0)
	s_barrier
; #define PG8_STAGE(bufoff, gbase, voff) do { if constexpr (!(Sched::CRIP & 2)) _Pragma("unroll") for (int _i = 0; _i < 2; ++_i) { unsigned _o = (voff)[_i]; asm volatile("" : "+v"(_o)); \
;         __builtin_amdgcn_global_load_lds((const unsigned*)((const char*)(gbase) + _o), (LAS unsigned*)(lds + (bufoff) + ldsw + _i * 8192), 16, 0, 0); } } while (0)
; #define PG8_LDA(dst, b, h) do { if constexpr (!(Sched::CRIP & 4)) _Pragma("unroll") for (int m = 0; m < 4; ++m) dst[m] = PG8_CAT(*(const LAS i32x4*)(lds + PG8_SA(b, h) + aoff + m * 2048), *(const LAS i32x4*)(lds + PG8_SA(b, h) + aoff + m * 2048 + 1024)); } while (0)
; #define PG8_LDB(dst, b, h) do { if constexpr (!(Sched::CRIP & 4)) _Pragma("unroll") for (int n = 0; n < 2; ++n) dst[n] = PG8_CAT(*(const LAS i32x4*)(lds + PG8_SB(b, h) + boff + n * 2048), *(const LAS i32x4*)(lds + PG8_SB(b, h) + boff + n * 2048 + 1024)); } while (0)
; #define PG8_WAIT_V(n) asm volatile("s_waitcnt vmcnt(" #n ")" ::: "memory")
; #define PG8_BAR __builtin_amdgcn_s_barrier()
; template <class Epi, class Sched>
; __device__ __forceinline__ void gemm_phase(LAS unsigned char* lds, const Sched& S, const Epi& E) {
;     ...
;         for (int t = 0; t < nt; t += 2) {
;             const bool last = (t == nt - 2);
;             const char* a1 = cA + PG8_KT(crot, t + 1);
;             const char* a2 = last ? nA + PG8_KT(nrot, 0) : cA + PG8_KT(crot, t + 2); const char* b2 = last ? nB + PG8_KT(nrot, 0) : cB + PG8_KT(crot, t + 2);
;             const char* a3 = last ? nA + PG8_KT(nrot, 1) : cA + PG8_KT(crot, t + 3); const char* b3 = last ? nB + PG8_KT(nrot, 1) : cB + PG8_KT(crot, t + 3);
;             int gi = 0;
;             if constexpr (Sched::GATHER) { if (t == 0 && has_next && tid < 256) gi = nxt.aidx[tid]; }
;             PG8_LDB(B0, 0, 0); PG8_LDB(B1, 0, 1); PG8_SCHED; PG8_LDA(At, 0, 0); PG8_STAGE(PG8_SA(1, 1), a1, vA[1]);
;             PG8_WAIT_V(8); PG8_WAIT_L(0); PG8_BAR; PG8_MMA(0, 0, At, B0); PG8_MMA(0, 1, At, B1); PG8_BAR2; PG8_SCHED;
;     ...
;             PG8_WAIT_V(8); PG8_WAIT_L(0); PG8_BAR; PG8_MMA(0, 0, At, B0); PG8_MMA(0, 1, At, B1); PG8_BAR2; PG8_SCHED;
;             PG8_LDA(At, 1, 1); PG8_STAGE(PG8_SB(1, 0), b3, voffB); PG8_STAGE(PG8_SB(1, 1), b3 + hstep, voffB); PG8_STAGE(PG8_SA(1, 0), a3, vA[0]);
;             PG8_WAIT_V(8); PG8_WAIT_L(0); PG8_BAR; PG8_MMA(1, 0, At, B0); PG8_MMA(1, 1, At, B1); PG8_BAR2; PG8_SCHED;
	s_setprio 1
	s_waitcnt lgkmcnt(0)
	s_nop 1
	v_mfma_scale_f32_16x16x128_f8f6f4 v[110:113], v[2:9], v[198:205], v[110:113], v185, v185 op_sel_hi:[0,0,0]
	v_mfma_scale_f32_16x16x128_f8f6f4 v[106:109], v[10:17], v[198:205], v[106:109], v185, v185 op_sel_hi:[0,0,0]
	v_mfma_scale_f32_16x16x128_f8f6f4 v[102:105], v[2:9], v[214:221], v[102:105], v185, v185 op_sel_hi:[0,0,0]
	v_mfma_scale_f32_16x16x128_f8f6f4 v[98:101], v[10:17], v[214:221], v[98:101], v185, v185 op_sel_hi:[0,0,0]
	v_mfma_scale_f32_16x16x128_f8f6f4 v[78:81], v[2:9], v[222:229], v[78:81], v185, v185 op_sel_hi:[0,0,0]
	v_mfma_scale_f32_16x16x128_f8f6f4 v[74:77], v[10:17], v[222:229], v[74:77], v185, v185 op_sel_hi:[0,0,0]
	v_mfma_scale_f32_16x16x128_f8f6f4 v[70:73], v[2:9], v[230:237], v[70:73], v185, v185 op_sel_hi:[0,0,0]
	v_mfma_scale_f32_16x16x128_f8f6f4 v[66:69], v[10:17], v[230:237], v[66:69], v185, v185 op_sel_hi:[0,0,0]
	s_setprio 0
	s_setprio 1
	s_nop 1
	v_mfma_scale_f32_16x16x128_f8f6f4 v[94:97], v[18:25], v[198:205], v[94:97], v185, v185 op_sel_hi:[0,0,0]
	v_mfma_scale_f32_16x16x128_f8f6f4 v[90:93], v[26:33], v[198:205], v[90:93], v185, v185 op_sel_hi:[0,0,0]
	v_mfma_scale_f32_16x16x128_f8f6f4 v[86:89], v[18:25], v[214:221], v[86:89], v185, v185 op_sel_hi:[0,0,0]
	v_mfma_scale_f32_16x16x128_f8f6f4 v[82:85], v[26:33], v[214:221], v[82:85], v185, v185 op_sel_hi:[0,0,0]
	v_mfma_scale_f32_16x16x128_f8f6f4 v[62:65], v[18:25], v[222:229], v[62:65], v185, v185 op_sel_hi:[0,0,0]
	v_mfma_scale_f32_16x16x128_f8f6f4 v[58:61], v[26:33], v[222:229], v[58:61], v185, v185 op_sel_hi:[0,0,0]
	v_mfma_scale_f32_16x16x128_f8f6f4 v[54:57], v[18:25], v[230:237], v[54:57], v185, v185 op_sel_hi:[0,0,0]
	v_mfma_scale_f32_16x16x128_f8f6f4 v[50:53], v[26:33], v[230:237], v[50:53], v185, v185 op_sel_hi:[0,0,0]
	s_setprio 0
	s_add_i32 s84, s84, 2
	s_addk_i32 s83, 0x100
.LBB0_807:
	s_barrier
	s_add_i32 s30, s83, 0xffffff00
	s_add_i32 s31, s83, 0xffffff80
	s_and_b32 s30, s30, 0x780
	s_and_b32 s31, s31, 0x780
	s_add_u32 s34, s26, s31
	s_addc_u32 s35, s27, 0
	s_add_u32 s40, s28, s31
	s_addc_u32 s41, s29, 0
	s_and_b32 s31, s83, 0x780
	s_add_u32 s53, s26, s31
	v_add_u32_e32 v2, s77, v186
	v_add_u32_e32 v22, s78, v186
	s_addc_u32 s85, s27, 0
	ds_read_b128 v[10:13], v2
	ds_read_b128 v[14:17], v2 offset:1024
	ds_read_b128 v[26:29], v2 offset:2048
	ds_read_b128 v[30:33], v2 offset:3072
	ds_read_b128 v[2:5], v22
	ds_read_b128 v[6:9], v22 offset:1024
	ds_read_b128 v[18:21], v22 offset:2048
	ds_read_b128 v[22:25], v22 offset:3072
	s_add_u32 s36, s28, s31
	s_addc_u32 s37, s29, 0
	s_add_u32 s54, s26, s30
	s_addc_u32 s55, s27, 0
	s_add_i32 s87, s77, s47
	s_add_i32 m0, s69, 0xc000
	s_add_i32 s86, s69, 0xe000
	s_add_i32 s52, s87, 0x2000
	s_cmp_eq_u32 s84, 12
	s_cselect_b32 s35, s17, s35
	s_cselect_b32 s34, s15, s34
	s_cselect_b32 s31, s80, s85
	s_cselect_b32 s30, s39, s53
	s_cselect_b32 s41, s38, s41
	s_cselect_b32 s40, s25, s40
	v_mov_b32_e32 v178, v183
	ds_read_b128 v[198:201], v188
	ds_read_b128 v[202:205], v188 offset:1024
	ds_read_b128 v[214:217], v188 offset:2048
	ds_read_b128 v[218:221], v188 offset:3072
	ds_read_b128 v[222:225], v188 offset:4096
	ds_read_b128 v[226:229], v188 offset:5120
	ds_read_b128 v[230:233], v188 offset:6144
	ds_read_b128 v[234:237], v188 offset:7168
	s_nop 0
	global_load_lds_dwordx4 v178, s[54:55]
	v_mov_b32_e32 v178, v184
	s_mov_b32 m0, s86
	s_nop 0
	global_load_lds_dwordx4 v178, s[54:55]
	s_waitcnt vmcnt(8)
	s_waitcnt lgkmcnt(0)
	s_barrier
	s_setprio 1
	s_waitcnt lgkmcnt(0)
	s_nop 1
	v_mfma_scale_f32_16x16x128_f8f6f4 v[174:177], v[10:17], v[198:205], v[174:177], v185, v185 op_sel_hi:[0,0,0]
	v_mfma_scale_f32_16x16x128_f8f6f4 v[170:173], v[26:33], v[198:205], v[170:173], v185, v185 op_sel_hi:[0,0,0]
	v_mfma_scale_f32_16x16x128_f8f6f4 v[166:169], v[10:17], v[214:221], v[166:169], v185, v185 op_sel_hi:[0,0,0]
	v_mfma_scale_f32_16x16x128_f8f6f4 v[162:165], v[26:33], v[214:221], v[162:165], v185, v185 op_sel_hi:[0,0,0]
	v_mfma_scale_f32_16x16x128_f8f6f4 v[142:145], v[10:17], v[222:229], v[142:145], v185, v185 op_sel_hi:[0,0,0]
	v_mfma_scale_f32_16x16x128_f8f6f4 v[138:141], v[26:33], v[222:229], v[138:141], v185, v185 op_sel_hi:[0,0,0]
	v_mfma_scale_f32_16x16x128_f8f6f4 v[134:137], v[10:17], v[230:237], v[134:137], v185, v185 op_sel_hi:[0,0,0]
	v_mfma_scale_f32_16x16x128_f8f6f4 v[130:133], v[26:33], v[230:237], v[130:133], v185, v185 op_sel_hi:[0,0,0]
	s_setprio 0
	s_setprio 1
	s_nop 1
	v_mfma_scale_f32_16x16x128_f8f6f4 v[158:161], v[2:9], v[198:205], v[158:161], v185, v185 op_sel_hi:[0,0,0]
	v_mfma_scale_f32_16x16x128_f8f6f4 v[154:157], v[18:25], v[198:205], v[154:157], v185, v185 op_sel_hi:[0,0,0]
	v_mfma_scale_f32_16x16x128_f8f6f4 v[150:153], v[2:9], v[214:221], v[150:153], v185, v185 op_sel_hi:[0,0,0]
	v_mfma_scale_f32_16x16x128_f8f6f4 v[146:149], v[18:25], v[214:221], v[146:149], v185, v185 op_sel_hi:[0,0,0]
	v_mfma_scale_f32_16x16x128_f8f6f4 v[126:129], v[2:9], v[222:229], v[126:129], v185, v185 op_sel_hi:[0,0,0]
	v_mfma_scale_f32_16x16x128_f8f6f4 v[122:125], v[18:25], v[222:229], v[122:125], v185, v185 op_sel_hi:[0,0,0]
	v_mfma_scale_f32_16x16x128_f8f6f4 v[118:121], v[2:9], v[230:237], v[118:121], v185, v185 op_sel_hi:[0,0,0]
	v_mfma_scale_f32_16x16x128_f8f6f4 v[114:117], v[18:25], v[230:237], v[114:117], v185, v185 op_sel_hi:[0,0,0]
	s_setprio 0
	s_barrier
; #define PG8_STAGE(bufoff, gbase, voff) do { if constexpr (!(Sched::CRIP & 2)) _Pragma("unroll") for (int _i = 0; _i < 2; ++_i) { unsigned _o = (voff)[_i]; asm volatile("" : "+v"(_o)); \
;         __builtin_amdgcn_global_load_lds((const unsigned*)((const char*)(gbase) + _o), (LAS unsigned*)(lds + (bufoff) + ldsw + _i * 8192), 16, 0, 0); } } while (0)
; #define PG8_LDA(dst, b, h) do { if constexpr (!(Sched::CRIP & 4)) _Pragma("unroll") for (int m = 0; m < 4; ++m) dst[m] = PG8_CAT(*(const LAS i32x4*)(lds + PG8_SA(b, h) + aoff + m * 2048), *(const LAS i32x4*)(lds + PG8_SA(b, h) + aoff + m * 2048 + 1024)); } while (0)
; #define PG8_LDB(dst, b, h) do { if constexpr (!(Sched::CRIP & 4)) _Pragma("unroll") for (int n = 0; n < 2; ++n) dst[n] = PG8_CAT(*(const LAS i32x4*)(lds + PG8_SB(b, h) + boff + n * 2048), *(const LAS i32x4*)(lds + PG8_SB(b, h) + boff + n * 2048 + 1024)); } while (0)
; #define PG8_WAIT_V(n) asm volatile("s_waitcnt vmcnt(" #n ")" ::: "memory")
; #define PG8_WAIT_L(n) asm volatile("s_waitcnt lgkmcnt(" #n ")" ::: "memory")
; #define PG8_BAR __builtin_amdgcn_s_barrier()
; #define PG8_SCHED __builtin_amdgcn_sched_barrier(0)
; template <class Epi, class Sched>
; __device__ __forceinline__ void gemm_phase(LAS unsigned char* lds, const Sched& S, const Epi& E) {
;     ...
;             PG8_LDA(At, 0, 1); PG8_STAGE(PG8_SB(0, 0), b2, voffB); PG8_STAGE(PG8_SB(0, 1), b2 + hstep, voffB); PG8_STAGE(PG8_SA(0, 0), a2, vA[0]);
;             PG8_WAIT_V(8); PG8_WAIT_L(0); PG8_BAR; PG8_MMA(1, 0, At, B0); PG8_MMA(1, 1, At, B1); PG8_BAR2; PG8_SCHED;
;             PG8_LDB(B0, 1, 0); PG8_LDB(B1, 1, 1); PG8_SCHED; PG8_LDA(At, 1, 0); PG8_STAGE(PG8_SA(0, 1), a2, vA[1]);
;             PG8_WAIT_V(8); PG8_WAIT_L(0); PG8_BAR; PG8_MMA(0, 0, At, B0); PG8_MMA(0, 1, At, B1); PG8_BAR2; PG8_SCHED;
	v_mov_b32_e32 v178, v1
	s_mov_b32 m0, s87
	ds_read_b128 v[198:201], v188 offset:16384
	ds_read_b128 v[202:205], v188 offset:17408
	ds_read_b128 v[214:217], v188 offset:18432
	ds_read_b128 v[218:221], v188 offset:19456
	ds_read_b128 v[222:225], v188 offset:20480
	ds_read_b128 v[226:229], v188 offset:21504
	ds_read_b128 v[230:233], v188 offset:22528
	ds_read_b128 v[234:237], v188 offset:23552
	s_cselect_b32 s36, s81, s36
	global_load_lds_dwordx4 v178, s[40:41]
	v_mov_b32_e32 v178, v180
	s_mov_b32 m0, s52
	s_cselect_b32 s37, s82, s37
	global_load_lds_dwordx4 v178, s[40:41]
	s_add_u32 s40, s40, 0x40000
	v_mov_b32_e32 v178, v1
	s_addc_u32 s41, s41, 0
	s_add_i32 s52, s78, s47
	s_mov_b32 m0, s52
	s_nop 0
	global_load_lds_dwordx4 v178, s[40:41]
	v_mov_b32_e32 v178, v180
	s_add_i32 m0, s52, 0x2000
	s_nop 0
	global_load_lds_dwordx4 v178, s[40:41]
	v_mov_b32_e32 v178, v181
	s_mov_b32 m0, s69
	s_nop 0
	global_load_lds_dwordx4 v178, s[34:35]
	v_mov_b32_e32 v178, v182
	s_mov_b32 m0, s70
	s_nop 0
	global_load_lds_dwordx4 v178, s[34:35]
	s_waitcnt vmcnt(8)
	s_waitcnt lgkmcnt(0)
	s_barrier
	s_setprio 1
	s_waitcnt lgkmcnt(0)
	s_nop 1
	v_mfma_scale_f32_16x16x128_f8f6f4 v[110:113], v[10:17], v[198:205], v[110:113], v185, v185 op_sel_hi:[0,0,0]
	v_mfma_scale_f32_16x16x128_f8f6f4 v[106:109], v[26:33], v[198:205], v[106:109], v185, v185 op_sel_hi:[0,0,0]
	v_mfma_scale_f32_16x16x128_f8f6f4 v[102:105], v[10:17], v[214:221], v[102:105], v185, v185 op_sel_hi:[0,0,0]
	v_mfma_scale_f32_16x16x128_f8f6f4 v[98:101], v[26:33], v[214:221], v[98:101], v185, v185 op_sel_hi:[0,0,0]
	v_mfma_scale_f32_16x16x128_f8f6f4 v[78:81], v[10:17], v[222:229], v[78:81], v185, v185 op_sel_hi:[0,0,0]
	v_mfma_scale_f32_16x16x128_f8f6f4 v[74:77], v[26:33], v[222:229], v[74:77], v185, v185 op_sel_hi:[0,0,0]
	v_mfma_scale_f32_16x16x128_f8f6f4 v[70:73], v[10:17], v[230:237], v[70:73], v185, v185 op_sel_hi:[0,0,0]
	v_mfma_scale_f32_16x16x128_f8f6f4 v[66:69], v[26:33], v[230:237], v[66:69], v185, v185 op_sel_hi:[0,0,0]
	s_setprio 0
	s_setprio 1
	s_nop 1
	v_mfma_scale_f32_16x16x128_f8f6f4 v[94:97], v[2:9], v[198:205], v[94:97], v185, v185 op_sel_hi:[0,0,0]
	v_mfma_scale_f32_16x16x128_f8f6f4 v[90:93], v[18:25], v[198:205], v[90:93], v185, v185 op_sel_hi:[0,0,0]
	v_mfma_scale_f32_16x16x128_f8f6f4 v[86:89], v[2:9], v[214:221], v[86:89], v185, v185 op_sel_hi:[0,0,0]
	v_mfma_scale_f32_16x16x128_f8f6f4 v[82:85], v[18:25], v[214:221], v[82:85], v185, v185 op_sel_hi:[0,0,0]
	v_mfma_scale_f32_16x16x128_f8f6f4 v[62:65], v[2:9], v[222:229], v[62:65], v185, v185 op_sel_hi:[0,0,0]
	v_mfma_scale_f32_16x16x128_f8f6f4 v[58:61], v[18:25], v[222:229], v[58:61], v185, v185 op_sel_hi:[0,0,0]
	v_mfma_scale_f32_16x16x128_f8f6f4 v[54:57], v[2:9], v[230:237], v[54:57], v185, v185 op_sel_hi:[0,0,0]
	v_mfma_scale_f32_16x16x128_f8f6f4 v[50:53], v[18:25], v[230:237], v[50:53], v185, v185 op_sel_hi:[0,0,0]
	s_setprio 0
	s_barrier
	s_add_i32 s40, 0, 0x18000
	s_add_i32 s41, 0, 0x1c000
	v_add_u32_e32 v14, s40, v186
	v_add_u32_e32 v30, s41, v186
	ds_read_b128 v[2:5], v14
	ds_read_b128 v[6:9], v14 offset:1024
	ds_read_b128 v[10:13], v14 offset:2048
	ds_read_b128 v[14:17], v14 offset:3072
	ds_read_b128 v[18:21], v30
	ds_read_b128 v[22:25], v30 offset:1024
	ds_read_b128 v[26:29], v30 offset:2048
	ds_read_b128 v[30:33], v30 offset:3072
	v_mov_b32_e32 v178, v183
	s_mov_b32 m0, s71
	ds_read_b128 v[198:201], v188 offset:32768
	ds_read_b128 v[202:205], v188 offset:33792
	ds_read_b128 v[214:217], v188 offset:34816
	ds_read_b128 v[218:221], v188 offset:35840
	ds_read_b128 v[222:225], v188 offset:36864
	ds_read_b128 v[226:229], v188 offset:37888
	ds_read_b128 v[230:233], v188 offset:38912
	ds_read_b128 v[234:237], v188 offset:39936
	s_nop 0
	global_load_lds_dwordx4 v178, s[34:35]
	v_mov_b32_e32 v178, v184
	s_mov_b32 m0, s72
	s_nop 0
	global_load_lds_dwordx4 v178, s[34:35]
	s_waitcnt vmcnt(8)
	s_waitcnt lgkmcnt(0)
	s_barrier
	s_setprio 1
	s_waitcnt lgkmcnt(0)
	s_nop 1
	v_mfma_scale_f32_16x16x128_f8f6f4 v[174:177], v[2:9], v[198:205], v[174:177], v185, v185 op_sel_hi:[0,0,0]
	v_mfma_scale_f32_16x16x128_f8f6f4 v[170:173], v[10:17], v[198:205], v[170:173], v185, v185 op_sel_hi:[0,0,0]
	v_mfma_scale_f32_16x16x128_f8f6f4 v[166:169], v[2:9], v[214:221], v[166:169], v185, v185 op_sel_hi:[0,0,0]
	v_mfma_scale_f32_16x16x128_f8f6f4 v[162:165], v[10:17], v[214:221], v[162:165], v185, v185 op_sel_hi:[0,0,0]
	v_mfma_scale_f32_16x16x128_f8f6f4 v[142:145], v[2:9], v[222:229], v[142:145], v185, v185 op_sel_hi:[0,0,0]
	v_mfma_scale_f32_16x16x128_f8f6f4 v[138:141], v[10:17], v[222:229], v[138:141], v185, v185 op_sel_hi:[0,0,0]
	v_mfma_scale_f32_16x16x128_f8f6f4 v[134:137], v[2:9], v[230:237], v[134:137], v185, v185 op_sel_hi:[0,0,0]
	v_mfma_scale_f32_16x16x128_f8f6f4 v[130:133], v[10:17], v[230:237], v[130:133], v185, v185 op_sel_hi:[0,0,0]
	s_setprio 0
	s_setprio 1
	s_nop 1
	v_mfma_scale_f32_16x16x128_f8f6f4 v[158:161], v[18:25], v[198:205], v[158:161], v185, v185 op_sel_hi:[0,0,0]
	v_mfma_scale_f32_16x16x128_f8f6f4 v[154:157], v[26:33], v[198:205], v[154:157], v185, v185 op_sel_hi:[0,0,0]
	v_mfma_scale_f32_16x16x128_f8f6f4 v[150:153], v[18:25], v[214:221], v[150:153], v185, v185 op_sel_hi:[0,0,0]
	v_mfma_scale_f32_16x16x128_f8f6f4 v[146:149], v[26:33], v[214:221], v[146:149], v185, v185 op_sel_hi:[0,0,0]
	v_mfma_scale_f32_16x16x128_f8f6f4 v[126:129], v[18:25], v[222:229], v[126:129], v185, v185 op_sel_hi:[0,0,0]
	v_mfma_scale_f32_16x16x128_f8f6f4 v[122:125], v[26:33], v[222:229], v[122:125], v185, v185 op_sel_hi:[0,0,0]
	v_mfma_scale_f32_16x16x128_f8f6f4 v[118:121], v[18:25], v[230:237], v[118:121], v185, v185 op_sel_hi:[0,0,0]
	v_mfma_scale_f32_16x16x128_f8f6f4 v[114:117], v[26:33], v[230:237], v[114:117], v185, v185 op_sel_hi:[0,0,0]
	s_setprio 0
	s_barrier
; __device__ __forceinline__ float sat8(float x) { return __builtin_amdgcn_fmed3f(x, -448.0f, 448.0f); }
; __device__ __forceinline__ unsigned pk4_fp8(float a, float b, float c, float d) { int v = 0; v = __builtin_amdgcn_cvt_pk_fp8_f32(a, b, v, false); v = __builtin_amdgcn_cvt_pk_fp8_f32(c, d, v, true); return (unsigned)v; }
; #define PG8_STAGE(bufoff, gbase, voff) do { if constexpr (!(Sched::CRIP & 2)) _Pragma("unroll") for (int _i = 0; _i < 2; ++_i) { unsigned _o = (voff)[_i]; asm volatile("" : "+v"(_o)); \
;         __builtin_amdgcn_global_load_lds((const unsigned*)((const char*)(gbase) + _o), (LAS unsigned*)(lds + (bufoff) + ldsw + _i * 8192), 16, 0, 0); } } while (0)
; template <class Epi, class Sched>
; __device__ __forceinline__ void gemm_phase(LAS unsigned char* lds, const Sched& S, const Epi& E) {
;     ...
;             PG8_LDA(At, 1, 1); PG8_STAGE(PG8_SB(1, 0), b3, voffB); PG8_STAGE(PG8_SB(1, 1), b3 + hstep, voffB); PG8_STAGE(PG8_SA(1, 0), a3, vA[0]);
;             PG8_WAIT_V(8); PG8_WAIT_L(0); PG8_BAR; PG8_MMA(1, 0, At, B0); PG8_MMA(1, 1, At, B1); PG8_BAR2; PG8_SCHED;
;             if constexpr (Sched::GATHER) { if (t == 0 && has_next && tid < 256) lidx[tid] = (tid < nxt.avalid) ? gi : 0; }
;         }
;         if constexpr (F8) asm volatile("s_nop 15\n\ts_nop 15" ::: "memory");
;         if (wr == 0) PG8_BAR;
;     __device__ __forceinline__ void operator()(const f32x4 (&acc)[2][2][4][2], const pg8::Unit& u, const Pre& q, int wr, int wc, int fr, int fq) const {
;     ...
;                 for (int bj = 0; bj < 2; ++bj) { unsigned lo[2], hi[2];
; #pragma unroll
;                     for (int mm = 0; mm < 2; ++mm) { const int m = 2 * mp + mm; const float gt = q.gt[ai][m] * FP8_SY;
;                         const f32x4 v0 = (acc[ai][bj][m][0] * DS + q.bv[bj][0]) * gt, v1 = (acc[ai][bj][m][1] * DS + q.bv[bj][1]) * gt;
;                         lo[mm] = pk4_fp8(sat8(v0[0]), sat8(v0[1]), sat8(v0[2]), sat8(v0[3])); hi[mm] = pk4_fp8(sat8(v1[0]), sat8(v1[1]), sat8(v1[2]), sat8(v1[3])); }
;                     const v2u r0 = __builtin_amdgcn_permlane16_swap(lo[0], lo[1], false, false), r1 = __builtin_amdgcn_permlane16_swap(hi[0], hi[1], false, false);
;                     unsigned char* rowp = y2 + (size_t)(u.pm * 256 + rl0 + ai * 128 + (2 * mp + (fq & 1)) * 16) * D + colw + bj * 128 + 16 * (fq >> 1);
;                     *(v4u*)rowp = (v4u){r0.x, r1.x, r0.y, r1.y}; }
	v_mov_b32_e32 v178, v1
	s_add_i32 s34, s40, s47
	ds_read_b128 v[198:201], v188 offset:49152
	ds_read_b128 v[202:205], v188 offset:50176
	ds_read_b128 v[214:217], v188 offset:51200
	ds_read_b128 v[218:221], v188 offset:52224
	ds_read_b128 v[222:225], v188 offset:53248
	ds_read_b128 v[226:229], v188 offset:54272
	ds_read_b128 v[230:233], v188 offset:55296
	ds_read_b128 v[234:237], v188 offset:56320
	s_mov_b32 m0, s34
	s_nop 0
	global_load_lds_dwordx4 v178, s[36:37]
	v_mov_b32_e32 v178, v180
	s_add_i32 m0, s34, 0x2000
	s_add_u32 s34, s36, 0x40000
	global_load_lds_dwordx4 v178, s[36:37]
	s_addc_u32 s35, s37, 0
	v_mov_b32_e32 v178, v1
	s_add_i32 s36, s41, s47
	s_mov_b32 m0, s36
	s_nop 0
	global_load_lds_dwordx4 v178, s[34:35]
	v_mov_b32_e32 v178, v180
	s_add_i32 m0, s36, 0x2000
	s_nop 0
	global_load_lds_dwordx4 v178, s[34:35]
	v_mov_b32_e32 v178, v181
	s_mov_b32 m0, s74
	s_nop 0
	global_load_lds_dwordx4 v178, s[30:31]
	v_mov_b32_e32 v178, v182
	s_mov_b32 m0, s75
	s_nop 0
	global_load_lds_dwordx4 v178, s[30:31]
	s_waitcnt vmcnt(8)
	s_waitcnt lgkmcnt(0)
	s_barrier
	s_setprio 1
	s_waitcnt lgkmcnt(0)
	s_nop 1
	v_mfma_scale_f32_16x16x128_f8f6f4 v[110:113], v[2:9], v[198:205], v[110:113], v185, v185 op_sel_hi:[0,0,0]
	v_mfma_scale_f32_16x16x128_f8f6f4 v[106:109], v[10:17], v[198:205], v[106:109], v185, v185 op_sel_hi:[0,0,0]
	v_mfma_scale_f32_16x16x128_f8f6f4 v[102:105], v[2:9], v[214:221], v[102:105], v185, v185 op_sel_hi:[0,0,0]
	v_mfma_scale_f32_16x16x128_f8f6f4 v[98:101], v[10:17], v[214:221], v[98:101], v185, v185 op_sel_hi:[0,0,0]
	v_mfma_scale_f32_16x16x128_f8f6f4 v[78:81], v[2:9], v[222:229], v[78:81], v185, v185 op_sel_hi:[0,0,0]
	v_mfma_scale_f32_16x16x128_f8f6f4 v[74:77], v[10:17], v[222:229], v[74:77], v185, v185 op_sel_hi:[0,0,0]
	v_mfma_scale_f32_16x16x128_f8f6f4 v[70:73], v[2:9], v[230:237], v[70:73], v185, v185 op_sel_hi:[0,0,0]
	v_mfma_scale_f32_16x16x128_f8f6f4 v[66:69], v[10:17], v[230:237], v[66:69], v185, v185 op_sel_hi:[0,0,0]
	s_setprio 0
	s_setprio 1
	s_nop 1
	v_mfma_scale_f32_16x16x128_f8f6f4 v[94:97], v[18:25], v[198:205], v[94:97], v185, v185 op_sel_hi:[0,0,0]
	v_mfma_scale_f32_16x16x128_f8f6f4 v[90:93], v[26:33], v[198:205], v[90:93], v185, v185 op_sel_hi:[0,0,0]
	v_mfma_scale_f32_16x16x128_f8f6f4 v[86:89], v[18:25], v[214:221], v[86:89], v185, v185 op_sel_hi:[0,0,0]
	v_mfma_scale_f32_16x16x128_f8f6f4 v[82:85], v[26:33], v[214:221], v[82:85], v185, v185 op_sel_hi:[0,0,0]
	v_mfma_scale_f32_16x16x128_f8f6f4 v[62:65], v[18:25], v[222:229], v[62:65], v185, v185 op_sel_hi:[0,0,0]
	v_mfma_scale_f32_16x16x128_f8f6f4 v[58:61], v[26:33], v[222:229], v[58:61], v185, v185 op_sel_hi:[0,0,0]
	v_mfma_scale_f32_16x16x128_f8f6f4 v[54:57], v[18:25], v[230:237], v[54:57], v185, v185 op_sel_hi:[0,0,0]
	v_mfma_scale_f32_16x16x128_f8f6f4 v[50:53], v[26:33], v[230:237], v[50:53], v185, v185 op_sel_hi:[0,0,0]
	s_setprio 0
	s_add_i32 s84, s84, 2
	s_addk_i32 s83, 0x100
	s_cmp_gt_u32 s84, 13
	s_cbranch_scc0 .LBB0_807
	s_nop 15
	s_nop 15
	s_and_b64 vcc, exec, s[8:9]
	s_cbranch_vccz .LBB0_810
	s_barrier
.LBB0_810:
	v_mov_b32_e32 v3, v0
	s_lshl_b32 s24, s24, 8
	v_readfirstlane_b32 s15, v3
	s_ashr_i32 s17, s15, 2
	s_lshr_b32 s15, s15, 1
	s_and_b32 s15, s15, 0x60
	s_andn2_b32 s17, s17, 63
	s_or_b32 s24, s15, s24
	s_lshl_b32 s15, s22, 8
	s_add_i32 s17, s17, s15
	v_and_or_b32 v2, v3, 31, s17
	v_lshrrev_b32_e32 v3, 1, v3
	s_waitcnt vmcnt(8)
	v_mul_f32_e32 v10, 0x42000000, v197
	v_pk_fma_f32 v[4:5], v[176:177], s[10:11], v[48:49] op_sel_hi:[1,0,1]
	v_pk_fma_f32 v[6:7], v[174:175], s[10:11], v[46:47] op_sel_hi:[1,0,1]
	v_and_b32_e32 v178, 16, v3
	v_ashrrev_i32_e32 v3, 31, v2
	v_pk_mul_f32 v[4:5], v[10:11], v[4:5] op_sel_hi:[0,1]
	v_pk_mul_f32 v[6:7], v[10:11], v[6:7] op_sel_hi:[0,1]
	v_pk_fma_f32 v[14:15], v[170:171], s[10:11], v[42:43] op_sel_hi:[1,0,1]
	v_lshlrev_b64 v[8:9], 11, v[2:3]
	v_pk_fma_f32 v[12:13], v[172:173], s[10:11], v[44:45] op_sel_hi:[1,0,1]
	v_pk_mul_f32 v[14:15], v[10:11], v[14:15] op_sel_hi:[0,1]
	v_med3_f32 v3, v6, s79, v189
	v_med3_f32 v6, v7, s79, v189
	v_med3_f32 v7, v4, s79, v189
	v_pk_mul_f32 v[12:13], v[10:11], v[12:13] op_sel_hi:[0,1]
	v_med3_f32 v11, v5, s79, v189
	v_cvt_pk_fp8_f32 v4, v3, v6
	v_med3_f32 v3, v14, s79, v189
	v_med3_f32 v6, v15, s79, v189
	v_cvt_pk_fp8_f32 v5, v3, v6
	v_med3_f32 v3, v12, s79, v189
	v_med3_f32 v6, v13, s79, v189
	v_cvt_pk_fp8_f32 v4, v7, v11 op_sel:[0,0,1]
	v_cvt_pk_fp8_f32 v5, v3, v6 op_sel:[0,0,1]
	v_mul_f32_e32 v12, 0x42000000, v196
	v_pk_fma_f32 v[6:7], v[168:169], s[10:11], v[48:49] op_sel_hi:[1,0,1]
	v_pk_fma_f32 v[14:15], v[166:167], s[10:11], v[46:47] op_sel_hi:[1,0,1]
	v_pk_mul_f32 v[6:7], v[12:13], v[6:7] op_sel_hi:[0,1]
	v_pk_mul_f32 v[14:15], v[12:13], v[14:15] op_sel_hi:[0,1]
	v_pk_fma_f32 v[16:17], v[164:165], s[10:11], v[44:45] op_sel_hi:[1,0,1]
	v_pk_fma_f32 v[18:19], v[162:163], s[10:11], v[42:43] op_sel_hi:[1,0,1]
	v_pk_mul_f32 v[16:17], v[12:13], v[16:17] op_sel_hi:[0,1]
	v_pk_mul_f32 v[18:19], v[12:13], v[18:19] op_sel_hi:[0,1]
	v_med3_f32 v3, v14, s79, v189
	v_med3_f32 v11, v15, s79, v189
	v_med3_f32 v13, v6, s79, v189
	v_med3_f32 v14, v7, s79, v189
	v_cvt_pk_fp8_f32 v6, v3, v11
	v_med3_f32 v3, v18, s79, v189
	v_med3_f32 v11, v19, s79, v189
	v_cvt_pk_fp8_f32 v7, v3, v11
	v_med3_f32 v3, v16, s79, v189
	v_med3_f32 v11, v17, s79, v189
	v_cvt_pk_fp8_f32 v6, v13, v14 op_sel:[0,0,1]
	v_cvt_pk_fp8_f32 v7, v3, v11 op_sel:[0,0,1]
	s_ashr_i32 s25, s24, 31
	v_lshl_add_u64 v[8:9], s[6:7], 0, v[8:9]
	v_lshl_add_u64 v[8:9], v[8:9], 0, s[24:25]
	v_permlane16_swap_b32_e32 v4, v6
	v_permlane16_swap_b32_e32 v5, v7
	v_lshl_add_u64 v[8:9], v[8:9], 0, v[178:179]
	global_store_dwordx4 v[8:9], v[4:7], off
; __device__ __forceinline__ float sat8(float x) { return __builtin_amdgcn_fmed3f(x, -448.0f, 448.0f); }
; __device__ __forceinline__ unsigned pk4_fp8(float a, float b, float c, float d) { int v = 0; v = __builtin_amdgcn_cvt_pk_fp8_f32(a, b, v, false); v = __builtin_amdgcn_cvt_pk_fp8_f32(c, d, v, true); return (unsigned)v; }
;     __device__ __forceinline__ void operator()(const f32x4 (&acc)[2][2][4][2], const pg8::Unit& u, const Pre& q, int wr, int wc, int fr, int fq) const {
;     ...
;                 for (int bj = 0; bj < 2; ++bj) { unsigned lo[2], hi[2];
; #pragma unroll
;                     for (int mm = 0; mm < 2; ++mm) { const int m = 2 * mp + mm; const float gt = q.gt[ai][m] * FP8_SY;
;                         const f32x4 v0 = (acc[ai][bj][m][0] * DS + q.bv[bj][0]) * gt, v1 = (acc[ai][bj][m][1] * DS + q.bv[bj][1]) * gt;
;                         lo[mm] = pk4_fp8(sat8(v0[0]), sat8(v0[1]), sat8(v0[2]), sat8(v0[3])); hi[mm] = pk4_fp8(sat8(v1[0]), sat8(v1[1]), sat8(v1[2]), sat8(v1[3])); }
;                     const v2u r0 = __builtin_amdgcn_permlane16_swap(lo[0], lo[1], false, false), r1 = __builtin_amdgcn_permlane16_swap(hi[0], hi[1], false, false);
;                     unsigned char* rowp = y2 + (size_t)(u.pm * 256 + rl0 + ai * 128 + (2 * mp + (fq & 1)) * 16) * D + colw + bj * 128 + 16 * (fq >> 1);
;                     *(v4u*)rowp = (v4u){r0.x, r1.x, r0.y, r1.y}; }
	v_pk_fma_f32 v[14:15], v[156:157], s[10:11], v[36:37] op_sel_hi:[1,0,1]
	v_pk_fma_f32 v[16:17], v[154:155], s[10:11], v[34:35] op_sel_hi:[1,0,1]
	v_pk_fma_f32 v[4:5], v[160:161], s[10:11], v[40:41] op_sel_hi:[1,0,1]
	v_pk_fma_f32 v[6:7], v[158:159], s[10:11], v[38:39] op_sel_hi:[1,0,1]
	v_pk_mul_f32 v[4:5], v[10:11], v[4:5] op_sel_hi:[0,1]
	v_pk_mul_f32 v[6:7], v[10:11], v[6:7] op_sel_hi:[0,1]
	v_pk_mul_f32 v[14:15], v[10:11], v[14:15] op_sel_hi:[0,1]
	v_pk_mul_f32 v[10:11], v[10:11], v[16:17] op_sel_hi:[0,1]
	v_med3_f32 v3, v6, s79, v189
	v_med3_f32 v6, v7, s79, v189
	v_med3_f32 v7, v4, s79, v189
	v_med3_f32 v13, v5, s79, v189
	v_cvt_pk_fp8_f32 v4, v3, v6
	v_med3_f32 v3, v10, s79, v189
	v_med3_f32 v6, v11, s79, v189
	v_cvt_pk_fp8_f32 v5, v3, v6
	v_med3_f32 v3, v14, s79, v189
	v_med3_f32 v6, v15, s79, v189
	v_cvt_pk_fp8_f32 v4, v7, v13 op_sel:[0,0,1]
	v_cvt_pk_fp8_f32 v5, v3, v6 op_sel:[0,0,1]
	v_pk_fma_f32 v[6:7], v[152:153], s[10:11], v[40:41] op_sel_hi:[1,0,1]
	v_pk_fma_f32 v[10:11], v[150:151], s[10:11], v[38:39] op_sel_hi:[1,0,1]
	v_pk_mul_f32 v[6:7], v[12:13], v[6:7] op_sel_hi:[0,1]
	v_pk_mul_f32 v[10:11], v[12:13], v[10:11] op_sel_hi:[0,1]
	v_pk_fma_f32 v[14:15], v[148:149], s[10:11], v[36:37] op_sel_hi:[1,0,1]
	v_pk_fma_f32 v[16:17], v[146:147], s[10:11], v[34:35] op_sel_hi:[1,0,1]
	v_pk_mul_f32 v[14:15], v[12:13], v[14:15] op_sel_hi:[0,1]
	v_pk_mul_f32 v[12:13], v[12:13], v[16:17] op_sel_hi:[0,1]
	v_med3_f32 v3, v10, s79, v189
	v_med3_f32 v10, v11, s79, v189
	v_med3_f32 v11, v6, s79, v189
	v_med3_f32 v16, v7, s79, v189
	v_cvt_pk_fp8_f32 v6, v3, v10
	v_med3_f32 v3, v12, s79, v189
	v_med3_f32 v10, v13, s79, v189
	v_cvt_pk_fp8_f32 v7, v3, v10
	v_med3_f32 v3, v14, s79, v189
	v_med3_f32 v10, v15, s79, v189
	v_cvt_pk_fp8_f32 v6, v11, v16 op_sel:[0,0,1]
	v_cvt_pk_fp8_f32 v7, v3, v10 op_sel:[0,0,1]
	v_mul_f32_e32 v10, 0x42000000, v195
	v_pk_fma_f32 v[14:15], v[138:139], s[10:11], v[42:43] op_sel_hi:[1,0,1]
	v_permlane16_swap_b32_e32 v4, v6
	v_permlane16_swap_b32_e32 v5, v7
	global_store_dwordx4 v[8:9], v[4:7], off offset:128
	v_pk_fma_f32 v[12:13], v[140:141], s[10:11], v[44:45] op_sel_hi:[1,0,1]
	v_pk_mul_f32 v[14:15], v[10:11], v[14:15] op_sel_hi:[0,1]
	v_or_b32_e32 v4, 32, v2
	v_ashrrev_i32_e32 v5, 31, v4
	v_lshlrev_b64 v[8:9], 11, v[4:5]
	v_pk_fma_f32 v[4:5], v[144:145], s[10:11], v[48:49] op_sel_hi:[1,0,1]
	v_pk_fma_f32 v[6:7], v[142:143], s[10:11], v[46:47] op_sel_hi:[1,0,1]
	v_pk_mul_f32 v[4:5], v[10:11], v[4:5] op_sel_hi:[0,1]
	v_pk_mul_f32 v[6:7], v[10:11], v[6:7] op_sel_hi:[0,1]
	v_med3_f32 v3, v6, s79, v189
	v_med3_f32 v6, v7, s79, v189
	v_med3_f32 v7, v4, s79, v189
	v_pk_mul_f32 v[12:13], v[10:11], v[12:13] op_sel_hi:[0,1]
	v_med3_f32 v11, v5, s79, v189
	v_cvt_pk_fp8_f32 v4, v3, v6
	v_med3_f32 v3, v14, s79, v189
	v_med3_f32 v6, v15, s79, v189
	v_cvt_pk_fp8_f32 v5, v3, v6
	v_med3_f32 v3, v12, s79, v189
	v_med3_f32 v6, v13, s79, v189
	v_cvt_pk_fp8_f32 v4, v7, v11 op_sel:[0,0,1]
	v_cvt_pk_fp8_f32 v5, v3, v6 op_sel:[0,0,1]
	v_mul_f32_e32 v12, 0x42000000, v194
	v_pk_fma_f32 v[6:7], v[136:137], s[10:11], v[48:49] op_sel_hi:[1,0,1]
	v_pk_fma_f32 v[14:15], v[134:135], s[10:11], v[46:47] op_sel_hi:[1,0,1]
	v_pk_mul_f32 v[6:7], v[12:13], v[6:7] op_sel_hi:[0,1]
	v_pk_mul_f32 v[14:15], v[12:13], v[14:15] op_sel_hi:[0,1]
	v_pk_fma_f32 v[16:17], v[132:133], s[10:11], v[44:45] op_sel_hi:[1,0,1]
	v_pk_fma_f32 v[18:19], v[130:131], s[10:11], v[42:43] op_sel_hi:[1,0,1]
	v_pk_mul_f32 v[16:17], v[12:13], v[16:17] op_sel_hi:[0,1]
	v_pk_mul_f32 v[18:19], v[12:13], v[18:19] op_sel_hi:[0,1]
	v_med3_f32 v3, v14, s79, v189
	v_med3_f32 v11, v15, s79, v189
	v_med3_f32 v13, v6, s79, v189
	v_med3_f32 v14, v7, s79, v189
	v_cvt_pk_fp8_f32 v6, v3, v11
	v_med3_f32 v3, v18, s79, v189
	v_med3_f32 v11, v19, s79, v189
	v_cvt_pk_fp8_f32 v7, v3, v11
	v_med3_f32 v3, v16, s79, v189
	v_med3_f32 v11, v17, s79, v189
	v_cvt_pk_fp8_f32 v6, v13, v14 op_sel:[0,0,1]
	v_cvt_pk_fp8_f32 v7, v3, v11 op_sel:[0,0,1]
	v_lshl_add_u64 v[8:9], s[6:7], 0, v[8:9]
	v_lshl_add_u64 v[8:9], v[8:9], 0, s[24:25]
	v_permlane16_swap_b32_e32 v4, v6
	v_permlane16_swap_b32_e32 v5, v7
	v_lshl_add_u64 v[8:9], v[8:9], 0, v[178:179]
	global_store_dwordx4 v[8:9], v[4:7], off
	v_pk_fma_f32 v[14:15], v[124:125], s[10:11], v[36:37] op_sel_hi:[1,0,1]
	v_pk_fma_f32 v[16:17], v[122:123], s[10:11], v[34:35] op_sel_hi:[1,0,1]
	v_pk_fma_f32 v[4:5], v[128:129], s[10:11], v[40:41] op_sel_hi:[1,0,1]
	v_pk_fma_f32 v[6:7], v[126:127], s[10:11], v[38:39] op_sel_hi:[1,0,1]
	v_pk_mul_f32 v[4:5], v[10:11], v[4:5] op_sel_hi:[0,1]
	v_pk_mul_f32 v[6:7], v[10:11], v[6:7] op_sel_hi:[0,1]
	v_pk_mul_f32 v[14:15], v[10:11], v[14:15] op_sel_hi:[0,1]
	v_pk_mul_f32 v[10:11], v[10:11], v[16:17] op_sel_hi:[0,1]
	v_med3_f32 v3, v6, s79, v189
	v_med3_f32 v6, v7, s79, v189
	v_med3_f32 v7, v4, s79, v189
	v_med3_f32 v13, v5, s79, v189
	v_cvt_pk_fp8_f32 v4, v3, v6
	v_med3_f32 v3, v10, s79, v189
	v_med3_f32 v6, v11, s79, v189
	v_cvt_pk_fp8_f32 v5, v3, v6
	v_med3_f32 v3, v14, s79, v189
	v_med3_f32 v6, v15, s79, v189
	v_cvt_pk_fp8_f32 v4, v7, v13 op_sel:[0,0,1]
	v_cvt_pk_fp8_f32 v5, v3, v6 op_sel:[0,0,1]
	v_pk_fma_f32 v[6:7], v[120:121], s[10:11], v[40:41] op_sel_hi:[1,0,1]
	v_pk_fma_f32 v[10:11], v[118:119], s[10:11], v[38:39] op_sel_hi:[1,0,1]
	v_pk_mul_f32 v[6:7], v[12:13], v[6:7] op_sel_hi:[0,1]
	v_pk_mul_f32 v[10:11], v[12:13], v[10:11] op_sel_hi:[0,1]
	v_pk_fma_f32 v[14:15], v[116:117], s[10:11], v[36:37] op_sel_hi:[1,0,1]
	v_pk_fma_f32 v[16:17], v[114:115], s[10:11], v[34:35] op_sel_hi:[1,0,1]
	v_pk_mul_f32 v[14:15], v[12:13], v[14:15] op_sel_hi:[0,1]
	v_pk_mul_f32 v[12:13], v[12:13], v[16:17] op_sel_hi:[0,1]
	v_med3_f32 v3, v10, s79, v189
; __device__ __forceinline__ float sat8(float x) { return __builtin_amdgcn_fmed3f(x, -448.0f, 448.0f); }
; __device__ __forceinline__ unsigned pk4_fp8(float a, float b, float c, float d) { int v = 0; v = __builtin_amdgcn_cvt_pk_fp8_f32(a, b, v, false); v = __builtin_amdgcn_cvt_pk_fp8_f32(c, d, v, true); return (unsigned)v; }
;     __device__ __forceinline__ void operator()(const f32x4 (&acc)[2][2][4][2], const pg8::Unit& u, const Pre& q, int wr, int wc, int fr, int fq) const {
;     ...
;                 for (int bj = 0; bj < 2; ++bj) { unsigned lo[2], hi[2];
; #pragma unroll
;                     for (int mm = 0; mm < 2; ++mm) { const int m = 2 * mp + mm; const float gt = q.gt[ai][m] * FP8_SY;
;                         const f32x4 v0 = (acc[ai][bj][m][0] * DS + q.bv[bj][0]) * gt, v1 = (acc[ai][bj][m][1] * DS + q.bv[bj][1]) * gt;
;                         lo[mm] = pk4_fp8(sat8(v0[0]), sat8(v0[1]), sat8(v0[2]), sat8(v0[3])); hi[mm] = pk4_fp8(sat8(v1[0]), sat8(v1[1]), sat8(v1[2]), sat8(v1[3])); }
;                     const v2u r0 = __builtin_amdgcn_permlane16_swap(lo[0], lo[1], false, false), r1 = __builtin_amdgcn_permlane16_swap(hi[0], hi[1], false, false);
;                     unsigned char* rowp = y2 + (size_t)(u.pm * 256 + rl0 + ai * 128 + (2 * mp + (fq & 1)) * 16) * D + colw + bj * 128 + 16 * (fq >> 1);
;                     *(v4u*)rowp = (v4u){r0.x, r1.x, r0.y, r1.y}; }
	v_med3_f32 v10, v11, s79, v189
	v_med3_f32 v11, v6, s79, v189
	v_med3_f32 v16, v7, s79, v189
	v_cvt_pk_fp8_f32 v6, v3, v10
	v_med3_f32 v3, v12, s79, v189
	v_med3_f32 v10, v13, s79, v189
	v_cvt_pk_fp8_f32 v7, v3, v10
	v_med3_f32 v3, v14, s79, v189
	v_med3_f32 v10, v15, s79, v189
	v_cvt_pk_fp8_f32 v6, v11, v16 op_sel:[0,0,1]
	v_cvt_pk_fp8_f32 v7, v3, v10 op_sel:[0,0,1]
	v_mul_f32_e32 v10, 0x42000000, v193
	v_pk_fma_f32 v[14:15], v[106:107], s[10:11], v[42:43] op_sel_hi:[1,0,1]
	v_permlane16_swap_b32_e32 v4, v6
	v_permlane16_swap_b32_e32 v5, v7
	global_store_dwordx4 v[8:9], v[4:7], off offset:128
	v_pk_fma_f32 v[12:13], v[108:109], s[10:11], v[44:45] op_sel_hi:[1,0,1]
	v_pk_mul_f32 v[14:15], v[10:11], v[14:15] op_sel_hi:[0,1]
	v_add_u32_e32 v4, 0x80, v2
	v_ashrrev_i32_e32 v5, 31, v4
	v_lshlrev_b64 v[8:9], 11, v[4:5]
	v_pk_fma_f32 v[4:5], v[112:113], s[10:11], v[48:49] op_sel_hi:[1,0,1]
	v_pk_fma_f32 v[6:7], v[110:111], s[10:11], v[46:47] op_sel_hi:[1,0,1]
	v_pk_mul_f32 v[4:5], v[10:11], v[4:5] op_sel_hi:[0,1]
	v_pk_mul_f32 v[6:7], v[10:11], v[6:7] op_sel_hi:[0,1]
	v_med3_f32 v3, v6, s79, v189
	v_med3_f32 v6, v7, s79, v189
	v_med3_f32 v7, v4, s79, v189
	v_pk_mul_f32 v[12:13], v[10:11], v[12:13] op_sel_hi:[0,1]
	v_med3_f32 v11, v5, s79, v189
	v_cvt_pk_fp8_f32 v4, v3, v6
	v_med3_f32 v3, v14, s79, v189
	v_med3_f32 v6, v15, s79, v189
	v_cvt_pk_fp8_f32 v5, v3, v6
	v_med3_f32 v3, v12, s79, v189
	v_med3_f32 v6, v13, s79, v189
	v_cvt_pk_fp8_f32 v4, v7, v11 op_sel:[0,0,1]
	v_cvt_pk_fp8_f32 v5, v3, v6 op_sel:[0,0,1]
	v_mul_f32_e32 v12, 0x42000000, v192
	v_pk_fma_f32 v[6:7], v[104:105], s[10:11], v[48:49] op_sel_hi:[1,0,1]
	v_pk_fma_f32 v[14:15], v[102:103], s[10:11], v[46:47] op_sel_hi:[1,0,1]
	v_pk_mul_f32 v[6:7], v[12:13], v[6:7] op_sel_hi:[0,1]
	v_pk_mul_f32 v[14:15], v[12:13], v[14:15] op_sel_hi:[0,1]
	v_pk_fma_f32 v[16:17], v[100:101], s[10:11], v[44:45] op_sel_hi:[1,0,1]
	v_pk_fma_f32 v[18:19], v[98:99], s[10:11], v[42:43] op_sel_hi:[1,0,1]
	v_pk_mul_f32 v[16:17], v[12:13], v[16:17] op_sel_hi:[0,1]
	v_pk_mul_f32 v[18:19], v[12:13], v[18:19] op_sel_hi:[0,1]
	v_med3_f32 v3, v14, s79, v189
	v_med3_f32 v11, v15, s79, v189
	v_med3_f32 v13, v6, s79, v189
	v_med3_f32 v14, v7, s79, v189
	v_cvt_pk_fp8_f32 v6, v3, v11
	v_med3_f32 v3, v18, s79, v189
	v_med3_f32 v11, v19, s79, v189
	v_cvt_pk_fp8_f32 v7, v3, v11
	v_med3_f32 v3, v16, s79, v189
	v_med3_f32 v11, v17, s79, v189
	v_cvt_pk_fp8_f32 v6, v13, v14 op_sel:[0,0,1]
	v_cvt_pk_fp8_f32 v7, v3, v11 op_sel:[0,0,1]
	v_lshl_add_u64 v[8:9], s[6:7], 0, v[8:9]
	v_lshl_add_u64 v[8:9], v[8:9], 0, s[24:25]
	v_permlane16_swap_b32_e32 v4, v6
	v_permlane16_swap_b32_e32 v5, v7
	v_lshl_add_u64 v[8:9], v[8:9], 0, v[178:179]
	global_store_dwordx4 v[8:9], v[4:7], off
	v_pk_fma_f32 v[14:15], v[92:93], s[10:11], v[36:37] op_sel_hi:[1,0,1]
	v_pk_fma_f32 v[16:17], v[90:91], s[10:11], v[34:35] op_sel_hi:[1,0,1]
	v_pk_fma_f32 v[4:5], v[96:97], s[10:11], v[40:41] op_sel_hi:[1,0,1]
	v_pk_fma_f32 v[6:7], v[94:95], s[10:11], v[38:39] op_sel_hi:[1,0,1]
	v_pk_mul_f32 v[4:5], v[10:11], v[4:5] op_sel_hi:[0,1]
	v_pk_mul_f32 v[6:7], v[10:11], v[6:7] op_sel_hi:[0,1]
	v_pk_mul_f32 v[14:15], v[10:11], v[14:15] op_sel_hi:[0,1]
	v_pk_mul_f32 v[10:11], v[10:11], v[16:17] op_sel_hi:[0,1]
	v_med3_f32 v3, v6, s79, v189
	v_med3_f32 v6, v7, s79, v189
	v_med3_f32 v7, v4, s79, v189
	v_med3_f32 v13, v5, s79, v189
	v_cvt_pk_fp8_f32 v4, v3, v6
	v_med3_f32 v3, v10, s79, v189
	v_med3_f32 v6, v11, s79, v189
	v_cvt_pk_fp8_f32 v5, v3, v6
	v_med3_f32 v3, v14, s79, v189
	v_med3_f32 v6, v15, s79, v189
	v_cvt_pk_fp8_f32 v4, v7, v13 op_sel:[0,0,1]
	v_cvt_pk_fp8_f32 v5, v3, v6 op_sel:[0,0,1]
	v_pk_fma_f32 v[6:7], v[88:89], s[10:11], v[40:41] op_sel_hi:[1,0,1]
	v_pk_fma_f32 v[10:11], v[86:87], s[10:11], v[38:39] op_sel_hi:[1,0,1]
	v_pk_mul_f32 v[6:7], v[12:13], v[6:7] op_sel_hi:[0,1]
	v_pk_mul_f32 v[10:11], v[12:13], v[10:11] op_sel_hi:[0,1]
	v_pk_fma_f32 v[14:15], v[84:85], s[10:11], v[36:37] op_sel_hi:[1,0,1]
	v_pk_fma_f32 v[16:17], v[82:83], s[10:11], v[34:35] op_sel_hi:[1,0,1]
	v_pk_mul_f32 v[14:15], v[12:13], v[14:15] op_sel_hi:[0,1]
	v_pk_mul_f32 v[12:13], v[12:13], v[16:17] op_sel_hi:[0,1]
	v_med3_f32 v3, v10, s79, v189
	v_med3_f32 v10, v11, s79, v189
	v_med3_f32 v11, v6, s79, v189
	v_med3_f32 v16, v7, s79, v189
	v_cvt_pk_fp8_f32 v6, v3, v10
	v_med3_f32 v3, v12, s79, v189
	v_med3_f32 v10, v13, s79, v189
	v_cvt_pk_fp8_f32 v7, v3, v10
	v_med3_f32 v3, v14, s79, v189
	v_med3_f32 v10, v15, s79, v189
	v_cvt_pk_fp8_f32 v6, v11, v16 op_sel:[0,0,1]
	v_cvt_pk_fp8_f32 v7, v3, v10 op_sel:[0,0,1]
	v_add_u32_e32 v2, 0xa0, v2
	v_ashrrev_i32_e32 v3, 31, v2
	v_permlane16_swap_b32_e32 v4, v6
	v_permlane16_swap_b32_e32 v5, v7
	global_store_dwordx4 v[8:9], v[4:7], off offset:128
	v_mul_f32_e32 v8, 0x42000000, v191
	v_pk_fma_f32 v[10:11], v[76:77], s[10:11], v[44:45] op_sel_hi:[1,0,1]
	v_lshlrev_b64 v[6:7], 11, v[2:3]
	v_pk_fma_f32 v[2:3], v[80:81], s[10:11], v[48:49] op_sel_hi:[1,0,1]
	v_pk_fma_f32 v[4:5], v[78:79], s[10:11], v[46:47] op_sel_hi:[1,0,1]
	v_pk_mul_f32 v[2:3], v[8:9], v[2:3] op_sel_hi:[0,1]
	v_pk_mul_f32 v[4:5], v[8:9], v[4:5] op_sel_hi:[0,1]
	v_pk_fma_f32 v[12:13], v[74:75], s[10:11], v[42:43] op_sel_hi:[1,0,1]
	v_pk_mul_f32 v[10:11], v[8:9], v[10:11] op_sel_hi:[0,1]
	v_pk_mul_f32 v[12:13], v[8:9], v[12:13] op_sel_hi:[0,1]
	v_med3_f32 v4, v4, s79, v189
	v_med3_f32 v5, v5, s79, v189
	v_med3_f32 v9, v2, s79, v189
	v_med3_f32 v14, v3, s79, v189
	v_cvt_pk_fp8_f32 v2, v4, v5
	v_med3_f32 v4, v12, s79, v189
; __device__ __forceinline__ float sat8(float x) { return __builtin_amdgcn_fmed3f(x, -448.0f, 448.0f); }
; __device__ __forceinline__ unsigned pk4_fp8(float a, float b, float c, float d) { int v = 0; v = __builtin_amdgcn_cvt_pk_fp8_f32(a, b, v, false); v = __builtin_amdgcn_cvt_pk_fp8_f32(c, d, v, true); return (unsigned)v; }
;     __device__ __forceinline__ void prefetch(const pg8::Unit& u, Pre& q) const {
;         int tz = threadIdx.x; asm volatile("" : "+v"(tz)); const int wid = tz >> 6, wr = wid >> 2, wc = wid & 3, fr = tz & 15, fq = (tz >> 4) & 3;
;         const int rl0 = wr * 64 + fr, col0 = u.pn * 256 + wc * 32 + 8 * fq;
;         const int mt = __builtin_amdgcn_readfirstlane(u.pm - tstart[u.e]);
;         const float* gp = sgate + (size_t)u.e * T + mt * 256;
; #pragma unroll
;         for (int bj = 0; bj < 2; ++bj)
; #pragma unroll
;             for (int n = 0; n < 2; ++n) q.bv[bj][n] = *(const f32x4*)(b_down + (size_t)u.e * D + col0 + bj * 128 + 4 * n);
; #pragma unroll
;         for (int ai = 0; ai < 2; ++ai)
; #pragma unroll
;             for (int m = 0; m < 4; ++m) q.gt[ai][m] = gp[rl0 + ai * 128 + m * 16];
;     }
;     __device__ __forceinline__ void operator()(const f32x4 (&acc)[2][2][4][2], const pg8::Unit& u, const Pre& q, int wr, int wc, int fr, int fq) const {
;     ...
;                 for (int bj = 0; bj < 2; ++bj) { unsigned lo[2], hi[2];
; #pragma unroll
;                     for (int mm = 0; mm < 2; ++mm) { const int m = 2 * mp + mm; const float gt = q.gt[ai][m] * FP8_SY;
;                         const f32x4 v0 = (acc[ai][bj][m][0] * DS + q.bv[bj][0]) * gt, v1 = (acc[ai][bj][m][1] * DS + q.bv[bj][1]) * gt;
;                         lo[mm] = pk4_fp8(sat8(v0[0]), sat8(v0[1]), sat8(v0[2]), sat8(v0[3])); hi[mm] = pk4_fp8(sat8(v1[0]), sat8(v1[1]), sat8(v1[2]), sat8(v1[3])); }
;                     const v2u r0 = __builtin_amdgcn_permlane16_swap(lo[0], lo[1], false, false), r1 = __builtin_amdgcn_permlane16_swap(hi[0], hi[1], false, false);
;                     unsigned char* rowp = y2 + (size_t)(u.pm * 256 + rl0 + ai * 128 + (2 * mp + (fq & 1)) * 16) * D + colw + bj * 128 + 16 * (fq >> 1);
;                     *(v4u*)rowp = (v4u){r0.x, r1.x, r0.y, r1.y}; }
	v_med3_f32 v5, v13, s79, v189
	v_cvt_pk_fp8_f32 v3, v4, v5
	v_med3_f32 v4, v10, s79, v189
	v_med3_f32 v5, v11, s79, v189
	v_mul_f32_e32 v10, 0x42000000, v190
	v_cvt_pk_fp8_f32 v3, v4, v5 op_sel:[0,0,1]
	v_pk_fma_f32 v[4:5], v[72:73], s[10:11], v[48:49] op_sel_hi:[1,0,1]
	v_pk_fma_f32 v[12:13], v[70:71], s[10:11], v[46:47] op_sel_hi:[1,0,1]
	v_cvt_pk_fp8_f32 v2, v9, v14 op_sel:[0,0,1]
	v_pk_mul_f32 v[4:5], v[10:11], v[4:5] op_sel_hi:[0,1]
	v_pk_mul_f32 v[12:13], v[10:11], v[12:13] op_sel_hi:[0,1]
	v_pk_fma_f32 v[14:15], v[68:69], s[10:11], v[44:45] op_sel_hi:[1,0,1]
	v_pk_fma_f32 v[16:17], v[66:67], s[10:11], v[42:43] op_sel_hi:[1,0,1]
	v_pk_mul_f32 v[14:15], v[10:11], v[14:15] op_sel_hi:[0,1]
	v_pk_mul_f32 v[16:17], v[10:11], v[16:17] op_sel_hi:[0,1]
	v_med3_f32 v9, v12, s79, v189
	v_med3_f32 v11, v13, s79, v189
	v_med3_f32 v12, v4, s79, v189
	v_med3_f32 v13, v5, s79, v189
	v_cvt_pk_fp8_f32 v4, v9, v11
	v_med3_f32 v9, v16, s79, v189
	v_med3_f32 v11, v17, s79, v189
	v_cvt_pk_fp8_f32 v5, v9, v11
	v_med3_f32 v9, v14, s79, v189
	v_med3_f32 v11, v15, s79, v189
	v_cvt_pk_fp8_f32 v4, v12, v13 op_sel:[0,0,1]
	v_cvt_pk_fp8_f32 v5, v9, v11 op_sel:[0,0,1]
	v_lshl_add_u64 v[6:7], s[6:7], 0, v[6:7]
	v_lshl_add_u64 v[6:7], v[6:7], 0, s[24:25]
	v_permlane16_swap_b32_e32 v2, v4
	v_permlane16_swap_b32_e32 v3, v5
	v_lshl_add_u64 v[6:7], v[6:7], 0, v[178:179]
	global_store_dwordx4 v[6:7], v[2:5], off
	v_pk_fma_f32 v[12:13], v[60:61], s[10:11], v[36:37] op_sel_hi:[1,0,1]
	v_pk_fma_f32 v[14:15], v[58:59], s[10:11], v[34:35] op_sel_hi:[1,0,1]
	v_pk_fma_f32 v[2:3], v[64:65], s[10:11], v[40:41] op_sel_hi:[1,0,1]
	v_pk_fma_f32 v[4:5], v[62:63], s[10:11], v[38:39] op_sel_hi:[1,0,1]
	v_pk_mul_f32 v[2:3], v[8:9], v[2:3] op_sel_hi:[0,1]
	v_pk_mul_f32 v[4:5], v[8:9], v[4:5] op_sel_hi:[0,1]
	v_pk_mul_f32 v[12:13], v[8:9], v[12:13] op_sel_hi:[0,1]
	v_pk_mul_f32 v[8:9], v[8:9], v[14:15] op_sel_hi:[0,1]
	v_med3_f32 v4, v4, s79, v189
	v_med3_f32 v5, v5, s79, v189
	v_med3_f32 v11, v2, s79, v189
	v_med3_f32 v14, v3, s79, v189
	v_cvt_pk_fp8_f32 v2, v4, v5
	v_med3_f32 v4, v8, s79, v189
	v_med3_f32 v5, v9, s79, v189
	v_cvt_pk_fp8_f32 v3, v4, v5
	v_med3_f32 v4, v12, s79, v189
	v_med3_f32 v5, v13, s79, v189
	v_pk_fma_f32 v[8:9], v[54:55], s[10:11], v[38:39] op_sel_hi:[1,0,1]
	v_cvt_pk_fp8_f32 v3, v4, v5 op_sel:[0,0,1]
	v_pk_fma_f32 v[4:5], v[56:57], s[10:11], v[40:41] op_sel_hi:[1,0,1]
	v_cvt_pk_fp8_f32 v2, v11, v14 op_sel:[0,0,1]
	v_pk_mul_f32 v[4:5], v[10:11], v[4:5] op_sel_hi:[0,1]
	v_pk_mul_f32 v[8:9], v[10:11], v[8:9] op_sel_hi:[0,1]
	v_pk_fma_f32 v[12:13], v[52:53], s[10:11], v[36:37] op_sel_hi:[1,0,1]
	v_pk_fma_f32 v[14:15], v[50:51], s[10:11], v[34:35] op_sel_hi:[1,0,1]
	v_pk_mul_f32 v[12:13], v[10:11], v[12:13] op_sel_hi:[0,1]
	v_pk_mul_f32 v[10:11], v[10:11], v[14:15] op_sel_hi:[0,1]
	v_med3_f32 v8, v8, s79, v189
	v_med3_f32 v9, v9, s79, v189
	v_med3_f32 v14, v4, s79, v189
	v_med3_f32 v15, v5, s79, v189
	v_cvt_pk_fp8_f32 v4, v8, v9
	v_med3_f32 v8, v10, s79, v189
	v_med3_f32 v9, v11, s79, v189
	v_cvt_pk_fp8_f32 v5, v8, v9
	v_med3_f32 v8, v12, s79, v189
	v_med3_f32 v9, v13, s79, v189
	v_cvt_pk_fp8_f32 v4, v14, v15 op_sel:[0,0,1]
	v_cvt_pk_fp8_f32 v5, v8, v9 op_sel:[0,0,1]
	s_andn2_b64 vcc, exec, s[0:1]
	s_mov_b64 s[0:1], -1
	v_permlane16_swap_b32_e32 v2, v4
	v_permlane16_swap_b32_e32 v3, v5
	v_readlane_b32 s38, v255, 28
	global_store_dwordx4 v[6:7], v[2:5], off offset:128
	s_cbranch_vccnz .LBB0_803
	s_lshl_b32 s0, s96, 2
	s_add_i32 s0, s0, 0
	s_add_i32 s0, s0, 0x27d00
	v_mov_b32_e32 v4, v0
	v_mov_b32_e32 v2, s0
	ds_read_b32 v3, v2
	v_lshrrev_b32_e32 v2, 1, v4
	s_ashr_i32 s97, s96, 31
	v_readlane_b32 s16, v255, 29
	v_and_b32_e32 v2, 0x78, v2
	s_waitcnt lgkmcnt(0)
	v_sub_u32_e32 v3, s14, v3
	s_lshl_b64 s[0:1], s[96:97], 17
	v_readfirstlane_b32 s15, v3
	s_lshl_b32 s34, s15, 8
	s_ashr_i32 s35, s34, 31
	s_lshl_b64 s[36:37], s[96:97], 13
	v_readlane_b32 s26, v255, 39
	v_readlane_b32 s28, v255, 41
	v_lshl_or_b32 v2, s12, 8, v2
	v_readlane_b32 s27, v255, 40
	v_readlane_b32 s29, v255, 42
	s_add_u32 s26, s28, s36
	v_ashrrev_i32_e32 v3, 31, v2
	s_addc_u32 s27, s29, s37
	v_readlane_b32 s17, v255, 30
	v_lshl_add_u64 v[2:3], v[2:3], 2, s[26:27]
	s_add_u32 s15, s11, s0
	v_ashrrev_i32_e32 v5, 2, v4
	global_load_dwordx4 v[42:45], v[2:3], off offset:16
	global_load_dwordx4 v[46:49], v[2:3], off
	global_load_dwordx4 v[34:37], v[2:3], off offset:528
	global_load_dwordx4 v[38:41], v[2:3], off offset:512
	v_and_b32_e32 v2, 15, v4
	s_addc_u32 s17, s42, s1
	s_lshl_b64 s[0:1], s[34:35], 2
	v_and_or_b32 v2, v5, s91, v2
	s_add_u32 s0, s15, s0
	s_addc_u32 s1, s17, s1
	v_ashrrev_i32_e32 v3, 31, v2
	v_lshl_add_u64 v[2:3], v[2:3], 2, s[0:1]
	global_load_dword v197, v[2:3], off
	global_load_dword v196, v[2:3], off offset:64
	global_load_dword v195, v[2:3], off offset:128
	global_load_dword v194, v[2:3], off offset:192
	global_load_dword v193, v[2:3], off offset:512
	global_load_dword v192, v[2:3], off offset:576
	global_load_dword v191, v[2:3], off offset:640
	global_load_dword v190, v[2:3], off offset:704
	s_andn2_b64 vcc, exec, s[4:5]
	v_readlane_b32 s18, v255, 31
	v_readlane_b32 s19, v255, 32
	v_readlane_b32 s20, v255, 33
	v_readlane_b32 s21, v255, 34
	v_readlane_b32 s22, v255, 35
	v_readlane_b32 s23, v255, 36
	v_readlane_b32 s24, v255, 37
	v_readlane_b32 s25, v255, 38
	v_readlane_b32 s30, v255, 43
	v_readlane_b32 s31, v255, 44
	s_mov_b32 s100, 0
	s_cbranch_vccnz .LBB0_802
	s_mov_b32 s100, 1
	s_branch .LBB0_802
